# P3 convpool LayerNorm: gain/bias vectors loaded once per phase into spare VGPRs instead of per-chunk pointer reload + dependent loads + waits
# baseline (speedup 1.0000x reference)
; #define LAS __attribute__((address_space(3)))
; __device__ __forceinline__ void phase_convpool(const Ctx& P, LAS unsigned char* lds, int vcu, int G) {
;     const int tid = threadIdx.x, lane = tid & 63, wave = __builtin_amdgcn_readfirstlane(tid >> 6);
;     const bf16_t* U = (const bf16_t*)(P.ws + WS_U); const bf16_t* Z = (const bf16_t*)(P.ws + WS_Z); bf16_t* Y0 = (bf16_t*)(P.ws + WS_Y0);
;     LAS float* tile = (LAS float*)lds;
;     const int c0 = 2 * tid;
;     f32x2 wk[31];
; #pragma unroll
;     for (int k = 0; k < 31; ++k) wk[k] = *(const f32x2*)(P.in[11] + (size_t)k * 1024 + c0);
;     const f32x2 cb = *(const f32x2*)(P.in[12] + c0);
;     ...
;             for (int j = 0; j < 4; ++j) { const int c = 4 * lane + 256 * j; const f32x4 g4 = *(const f32x4*)(P.in[13] + c), b4 = *(const f32x4*)(P.in[14] + c); f32x4 y = v[j] * rstd * g4 + b4;
.LBB0_671:
	s_or_b64 exec, exec, s[40:41]
	s_mov_b64 s[2:3], s[0:1]
	s_nop 0
	v_mov_b64_e32 v[2:3], s[2:3]
	flat_load_dword v1, v[2:3] offset:296
	s_waitcnt vmcnt(0) lgkmcnt(0)
	v_cmp_gt_i32_e32 vcc, 4, v1
	s_and_saveexec_b64 s[2:3], vcc
	s_cbranch_execz .LBB0_1122
	s_mov_b64 s[4:5], s[0:1]
	s_nop 0
	v_mov_b64_e32 v[2:3], s[4:5]
	flat_load_dword v1, v[2:3] offset:300
	s_waitcnt vmcnt(0) lgkmcnt(0)
	v_cmp_lt_i32_e32 vcc, 3, v1
	s_and_b64 exec, exec, vcc
	s_cbranch_execz .LBB0_1122
	v_mov_b64_e32 v[250:251], s[0:1]
	flat_load_dwordx4 v[246:249], v[250:251] offset:104
	v_and_b32_e32 v252, 63, v0
	v_lshlrev_b32_e32 v252, 4, v252
	v_mov_b32_e32 v253, 0
	s_waitcnt vmcnt(0) lgkmcnt(0)
	v_lshl_add_u64 v[254:255], v[246:247], 0, v[252:253]
	v_lshl_add_u64 v[250:251], v[248:249], 0, v[252:253]
	global_load_dwordx4 v[222:225], v[254:255], off
	global_load_dwordx4 v[226:229], v[254:255], off offset:1024
	global_load_dwordx4 v[230:233], v[254:255], off offset:2048
	global_load_dwordx4 v[234:237], v[254:255], off offset:3072
	global_load_dwordx4 v[238:241], v[250:251], off
	global_load_dwordx4 v[242:245], v[250:251], off offset:1024
	global_load_dwordx4 v[246:249], v[250:251], off offset:2048
	global_load_dwordx4 v[250:253], v[250:251], off offset:3072
	s_waitcnt vmcnt(0)
	s_mov_b64 s[4:5], s[0:1]
	s_mov_b64 s[6:7], s[0:1]
	s_cmpk_gt_i32 s33, 0x21f
	v_readfirstlane_b32 s10, v0
	s_cbranch_scc1 .LBB0_1122
	v_mov_b64_e32 v[2:3], s[4:5]
	flat_load_dwordx4 v[2:5], v[2:3] offset:88
	v_lshlrev_b32_e32 v6, 3, v0
	v_mov_b32_e32 v7, 0
	s_add_u32 s12, s36, 0x28ec0000
	s_addc_u32 s13, s37, 0
	s_cmpk_gt_u32 s10, 0x7f
	v_and_b32_e32 v78, 63, v0
	s_cselect_b64 s[6:7], -1, 0
	s_lshr_b32 s9, s10, 7
	s_lshr_b32 s10, s10, 4
	s_mov_b64 s[14:15], 0x38dc0000
	v_add_u32_e32 v1, 0, v6
	s_and_b32 s18, s10, 0xffffffc
	v_lshl_add_u32 v188, v78, 4, 0
	s_or_b32 s20, s18, 1
	s_or_b32 s22, s18, 2
	s_or_b32 s24, s10, 3
	v_add_u32_e32 v189, 0x10000, v1
	v_add_u32_e32 v190, 0x11000, v1
	v_add_u32_e32 v191, 0x12000, v1
	v_add_u32_e32 v192, 0x13000, v1
	v_add_u32_e32 v193, 0x14000, v1
	v_add_u32_e32 v194, 0x15000, v1
	v_add_u32_e32 v195, 0x16000, v1
	v_add_u32_e32 v196, 0x17000, v1
	v_add_u32_e32 v197, 0x18000, v1
	v_add_u32_e32 v198, 0x19000, v1
	v_add_u32_e32 v199, 0x1a000, v1
	v_add_u32_e32 v200, 0x1b000, v1
	v_add_u32_e32 v201, 0x1c000, v1
	v_add_u32_e32 v202, 0x1d000, v1
	v_add_u32_e32 v203, 0x1e000, v1
	v_add_u32_e32 v204, 0x1f000, v1
	s_lshl_b32 s19, s18, 12
	s_lshl_b32 s21, s20, 12
	s_lshl_b32 s23, s22, 12
	s_lshl_b32 s25, s24, 12
	s_lshl_b32 s26, s33, 5
	s_lshl_b32 s27, s39, 5
	s_movk_i32 s28, 0xfe0
	s_movk_i32 s29, 0x100
	v_mov_b32_e32 v205, 0x358637bd
	s_mov_b32 s30, s33
	s_waitcnt vmcnt(0) lgkmcnt(0)
	v_lshl_add_u64 v[2:3], v[2:3], 0, v[6:7]
	v_add_co_u32_e32 v16, vcc, 0x1000, v2
	s_nop 1
	v_addc_co_u32_e32 v17, vcc, 0, v3, vcc
	v_add_co_u32_e32 v18, vcc, 0x2000, v2
	s_nop 1
	v_addc_co_u32_e32 v19, vcc, 0, v3, vcc
	v_add_co_u32_e32 v20, vcc, 0x3000, v2
	s_nop 1
	v_addc_co_u32_e32 v21, vcc, 0, v3, vcc
	v_add_co_u32_e32 v24, vcc, 0x4000, v2
	global_load_dwordx2 v[8:9], v[2:3], off
	global_load_dwordx2 v[10:11], v[16:17], off
	global_load_dwordx2 v[12:13], v[18:19], off
	global_load_dwordx2 v[14:15], v[20:21], off
	v_addc_co_u32_e32 v25, vcc, 0, v3, vcc
	v_add_co_u32_e32 v26, vcc, 0x5000, v2
	s_nop 1
	v_addc_co_u32_e32 v27, vcc, 0, v3, vcc
	v_add_co_u32_e32 v28, vcc, 0x6000, v2
	s_nop 1
	v_addc_co_u32_e32 v29, vcc, 0, v3, vcc
	v_add_co_u32_e32 v30, vcc, 0x7000, v2
	s_nop 1
	v_addc_co_u32_e32 v31, vcc, 0, v3, vcc
	v_add_co_u32_e32 v32, vcc, 0x8000, v2
	global_load_dwordx2 v[16:17], v[24:25], off
	global_load_dwordx2 v[18:19], v[26:27], off
	global_load_dwordx2 v[20:21], v[28:29], off
	global_load_dwordx2 v[22:23], v[30:31], off
	v_addc_co_u32_e32 v33, vcc, 0, v3, vcc
	v_add_co_u32_e32 v34, vcc, 0x9000, v2
	s_nop 1
	v_addc_co_u32_e32 v35, vcc, 0, v3, vcc
	v_add_co_u32_e32 v36, vcc, 0xa000, v2
	s_nop 1
	v_addc_co_u32_e32 v37, vcc, 0, v3, vcc
	v_add_co_u32_e32 v38, vcc, 0xb000, v2
	s_nop 1
	v_addc_co_u32_e32 v39, vcc, 0, v3, vcc
	v_add_co_u32_e32 v40, vcc, 0xc000, v2
	global_load_dwordx2 v[24:25], v[32:33], off
	global_load_dwordx2 v[26:27], v[34:35], off
	global_load_dwordx2 v[28:29], v[36:37], off
	global_load_dwordx2 v[30:31], v[38:39], off
	v_addc_co_u32_e32 v41, vcc, 0, v3, vcc
	v_add_co_u32_e32 v42, vcc, 0xd000, v2
	s_nop 1
	v_addc_co_u32_e32 v43, vcc, 0, v3, vcc
	v_add_co_u32_e32 v44, vcc, 0xe000, v2
	s_nop 1
	v_addc_co_u32_e32 v45, vcc, 0, v3, vcc
	v_add_co_u32_e32 v46, vcc, 0xf000, v2
	s_nop 1
	v_addc_co_u32_e32 v47, vcc, 0, v3, vcc
	v_add_co_u32_e32 v48, vcc, 0x10000, v2
	global_load_dwordx2 v[32:33], v[40:41], off
	global_load_dwordx2 v[34:35], v[42:43], off
	global_load_dwordx2 v[36:37], v[44:45], off
	global_load_dwordx2 v[38:39], v[46:47], off
	v_addc_co_u32_e32 v49, vcc, 0, v3, vcc
	v_add_co_u32_e32 v50, vcc, 0x11000, v2
	s_nop 1
	v_addc_co_u32_e32 v51, vcc, 0, v3, vcc
	v_add_co_u32_e32 v52, vcc, 0x12000, v2
	s_nop 1
	v_addc_co_u32_e32 v53, vcc, 0, v3, vcc
	v_add_co_u32_e32 v54, vcc, 0x13000, v2
	s_nop 1
	v_addc_co_u32_e32 v55, vcc, 0, v3, vcc
	v_add_co_u32_e32 v56, vcc, 0x14000, v2
	global_load_dwordx2 v[40:41], v[48:49], off
	global_load_dwordx2 v[42:43], v[50:51], off
	global_load_dwordx2 v[44:45], v[52:53], off
	global_load_dwordx2 v[46:47], v[54:55], off
	v_addc_co_u32_e32 v57, vcc, 0, v3, vcc
	v_add_co_u32_e32 v58, vcc, 0x15000, v2
	s_nop 1
	v_addc_co_u32_e32 v59, vcc, 0, v3, vcc
	v_add_co_u32_e32 v60, vcc, 0x16000, v2
	s_nop 1
	v_addc_co_u32_e32 v61, vcc, 0, v3, vcc
	v_add_co_u32_e32 v62, vcc, 0x17000, v2
	s_nop 1
	v_addc_co_u32_e32 v63, vcc, 0, v3, vcc
; #define LAS __attribute__((address_space(3)))
; __device__ __forceinline__ float bf_lo(unsigned w) { return __uint_as_float(w << 16); }
; __device__ __forceinline__ float bf_hi(unsigned w) { return __uint_as_float(w & 0xffff0000u); }
; __device__ __forceinline__ void phase_convpool(const Ctx& P, LAS unsigned char* lds, int vcu, int G) {
;     ...
; #pragma unroll
;     for (int k = 0; k < 31; ++k) wk[k] = *(const f32x2*)(P.in[11] + (size_t)k * 1024 + c0);
;     const f32x2 cb = *(const f32x2*)(P.in[12] + c0);
;     constexpr int NU = 4 * 128 + 4 * 8;
;     for (int un = vcu; un < NU; un += G) {
;         int rowbase, L, t0;
;         if (un < 512) { rowbase = (un >> 7) * SEQ; L = SEQ; t0 = (un & 127) * 32; } else { const int q = un - 512; rowbase = ML + (q >> 3) * CTXL; L = CTXL; t0 = (q & 7) * 32; }
;         const int grp = wave >> 1;
;         if (grp == 0) pool_tile<2>(U, Y0, rowbase, L, t0, c0); else if (grp == 1) pool_tile<4>(U, Y0, rowbase, L, t0, c0); else if (grp == 2) pool_tile<8>(U, Y0, rowbase, L, t0, c0); else pool_tile<16>(U, Y0, rowbase, L, t0, c0);
;         {
;             f32x2 zr[62];
; #pragma unroll
;             for (int q = 0; q < 62; ++q) { const int j = t0 - 15 + q; unsigned w = 0u; if (j >= 0 && j < L) w = *(const unsigned*)(Z + (size_t)(rowbase + j) * 1024 + c0); zr[q] = (f32x2){bf_lo(w), bf_hi(w)}; }
; #pragma unroll
;             for (int tt = 0; tt < 32; ++tt) { f32x2 a = cb;
; #pragma unroll
;                 for (int k = 0; k < 31; ++k) a += wk[k] * zr[tt + k];
;                 *(LAS f32x2*)(tile + tt * 1024 + c0) = a; }
	v_add_co_u32_e32 v64, vcc, 0x18000, v2
	global_load_dwordx2 v[48:49], v[56:57], off
	global_load_dwordx2 v[50:51], v[58:59], off
	global_load_dwordx2 v[52:53], v[60:61], off
	global_load_dwordx2 v[54:55], v[62:63], off
	v_addc_co_u32_e32 v65, vcc, 0, v3, vcc
	v_add_co_u32_e32 v66, vcc, 0x19000, v2
	s_nop 1
	v_addc_co_u32_e32 v67, vcc, 0, v3, vcc
	v_add_co_u32_e32 v68, vcc, 0x1a000, v2
	s_nop 1
	v_addc_co_u32_e32 v69, vcc, 0, v3, vcc
	v_add_co_u32_e32 v70, vcc, 0x1b000, v2
	s_nop 1
	v_addc_co_u32_e32 v71, vcc, 0, v3, vcc
	global_load_dwordx2 v[56:57], v[64:65], off
	global_load_dwordx2 v[58:59], v[66:67], off
	global_load_dwordx2 v[60:61], v[68:69], off
	global_load_dwordx2 v[62:63], v[70:71], off
	v_add_co_u32_e32 v70, vcc, 0x1c000, v2
	s_nop 1
	v_addc_co_u32_e32 v71, vcc, 0, v3, vcc
	v_add_co_u32_e32 v72, vcc, 0x1d000, v2
	s_nop 1
	v_addc_co_u32_e32 v73, vcc, 0, v3, vcc
	v_add_co_u32_e32 v2, vcc, 0x1e000, v2
	s_nop 1
	v_addc_co_u32_e32 v3, vcc, 0, v3, vcc
	global_load_dwordx2 v[64:65], v[70:71], off
	global_load_dwordx2 v[66:67], v[72:73], off
	global_load_dwordx2 v[68:69], v[2:3], off
	v_lshl_add_u64 v[2:3], v[4:5], 0, v[6:7]
	global_load_dwordx2 v[70:71], v[2:3], off
	v_lshlrev_b32_e32 v2, 2, v0
	v_mov_b32_e32 v3, v7
	v_lshl_add_u64 v[4:5], s[36:37], 0, v[2:3]
	v_lshl_add_u64 v[74:75], s[12:13], 0, v[2:3]
	v_lshlrev_b32_e32 v2, 2, v78
	v_lshlrev_b32_e32 v6, 3, v78
	v_lshl_add_u64 v[72:73], v[4:5], 0, s[14:15]
	s_mov_b64 s[14:15], 0x3afc0000
	v_lshl_add_u64 v[78:79], s[12:13], 0, v[6:7]
	v_lshlrev_b32_e32 v6, 2, v2
	v_mbcnt_lo_u32_b32 v2, -1, 0
	v_lshl_add_u64 v[76:77], v[4:5], 0, s[14:15]
	v_mbcnt_hi_u32_b32 v206, -1, v2
	s_branch .LBB0_676
.LBB0_675:
	s_waitcnt vmcnt(0)
	v_lshlrev_b32_e32 v220, 16, v136
	v_and_b32_e32 v221, 0xffff0000, v136
	v_lshlrev_b32_e32 v212, 16, v210
	v_and_b32_e32 v213, 0xffff0000, v210
	v_lshlrev_b32_e32 v218, 16, v137
	v_and_b32_e32 v219, 0xffff0000, v137
	v_lshlrev_b32_e32 v136, 16, v211
	v_and_b32_e32 v137, 0xffff0000, v211
	v_pk_fma_f32 v[210:211], v[8:9], v[220:221], v[70:71]
	v_lshlrev_b32_e32 v214, 16, v209
	v_and_b32_e32 v215, 0xffff0000, v209
	v_lshlrev_b32_e32 v216, 16, v208
	v_and_b32_e32 v217, 0xffff0000, v208
	v_lshlrev_b32_e32 v208, 16, v207
	v_and_b32_e32 v209, 0xffff0000, v207
	v_pk_fma_f32 v[210:211], v[10:11], v[218:219], v[210:211]
	v_pk_fma_f32 v[218:219], v[8:9], v[218:219], v[70:71]
	v_pk_fma_f32 v[210:211], v[12:13], v[208:209], v[210:211]
	v_pk_fma_f32 v[218:219], v[10:11], v[208:209], v[218:219]
	v_pk_fma_f32 v[210:211], v[14:15], v[216:217], v[210:211]
	v_pk_fma_f32 v[218:219], v[12:13], v[216:217], v[218:219]
	v_lshlrev_b32_e32 v186, 16, v187
	v_pk_fma_f32 v[218:219], v[14:15], v[214:215], v[218:219]
	v_and_b32_e32 v187, 0xffff0000, v187
	v_pk_fma_f32 v[210:211], v[16:17], v[214:215], v[210:211]
	v_pk_fma_f32 v[218:219], v[16:17], v[212:213], v[218:219]
	v_lshlrev_b32_e32 v184, 16, v185
	v_and_b32_e32 v185, 0xffff0000, v185
	v_pk_fma_f32 v[210:211], v[18:19], v[212:213], v[210:211]
	v_pk_fma_f32 v[218:219], v[18:19], v[186:187], v[218:219]
	v_lshlrev_b32_e32 v182, 16, v183
	v_and_b32_e32 v183, 0xffff0000, v183
	v_pk_fma_f32 v[210:211], v[20:21], v[186:187], v[210:211]
	v_pk_fma_f32 v[218:219], v[20:21], v[184:185], v[218:219]
	v_lshlrev_b32_e32 v180, 16, v181
	v_and_b32_e32 v181, 0xffff0000, v181
	v_pk_fma_f32 v[210:211], v[22:23], v[184:185], v[210:211]
	v_pk_fma_f32 v[218:219], v[22:23], v[182:183], v[218:219]
	v_lshlrev_b32_e32 v178, 16, v179
	v_and_b32_e32 v179, 0xffff0000, v179
	v_pk_fma_f32 v[210:211], v[24:25], v[182:183], v[210:211]
	v_pk_fma_f32 v[218:219], v[24:25], v[180:181], v[218:219]
	v_lshlrev_b32_e32 v176, 16, v177
	v_and_b32_e32 v177, 0xffff0000, v177
	v_pk_fma_f32 v[210:211], v[26:27], v[180:181], v[210:211]
	v_pk_fma_f32 v[218:219], v[26:27], v[178:179], v[218:219]
	v_lshlrev_b32_e32 v174, 16, v175
	v_and_b32_e32 v175, 0xffff0000, v175
	v_pk_fma_f32 v[210:211], v[28:29], v[178:179], v[210:211]
	v_pk_fma_f32 v[218:219], v[28:29], v[176:177], v[218:219]
	v_lshlrev_b32_e32 v172, 16, v173
	v_and_b32_e32 v173, 0xffff0000, v173
	v_pk_fma_f32 v[210:211], v[30:31], v[176:177], v[210:211]
	v_pk_fma_f32 v[218:219], v[30:31], v[174:175], v[218:219]
	v_lshlrev_b32_e32 v170, 16, v171
	v_and_b32_e32 v171, 0xffff0000, v171
	v_pk_fma_f32 v[210:211], v[32:33], v[174:175], v[210:211]
	v_pk_fma_f32 v[218:219], v[32:33], v[172:173], v[218:219]
	v_lshlrev_b32_e32 v168, 16, v169
	v_and_b32_e32 v169, 0xffff0000, v169
	v_pk_fma_f32 v[210:211], v[34:35], v[172:173], v[210:211]
	v_pk_fma_f32 v[218:219], v[34:35], v[170:171], v[218:219]
	v_lshlrev_b32_e32 v166, 16, v167
	v_and_b32_e32 v167, 0xffff0000, v167
	v_pk_fma_f32 v[210:211], v[36:37], v[170:171], v[210:211]
	v_pk_fma_f32 v[218:219], v[36:37], v[168:169], v[218:219]
	v_lshlrev_b32_e32 v164, 16, v165
	v_and_b32_e32 v165, 0xffff0000, v165
	v_pk_fma_f32 v[210:211], v[38:39], v[168:169], v[210:211]
	v_pk_fma_f32 v[218:219], v[38:39], v[166:167], v[218:219]
	v_lshlrev_b32_e32 v162, 16, v163
	v_and_b32_e32 v163, 0xffff0000, v163
	v_pk_fma_f32 v[210:211], v[40:41], v[166:167], v[210:211]
	v_pk_fma_f32 v[218:219], v[40:41], v[164:165], v[218:219]
	v_lshlrev_b32_e32 v160, 16, v161
	v_and_b32_e32 v161, 0xffff0000, v161
	v_pk_fma_f32 v[210:211], v[42:43], v[164:165], v[210:211]
	v_pk_fma_f32 v[218:219], v[42:43], v[162:163], v[218:219]
	v_lshlrev_b32_e32 v158, 16, v159
	v_and_b32_e32 v159, 0xffff0000, v159
	v_pk_fma_f32 v[210:211], v[44:45], v[162:163], v[210:211]
	v_pk_fma_f32 v[218:219], v[44:45], v[160:161], v[218:219]
	v_lshlrev_b32_e32 v156, 16, v157
	v_and_b32_e32 v157, 0xffff0000, v157
	v_pk_fma_f32 v[210:211], v[46:47], v[160:161], v[210:211]
; #define LAS __attribute__((address_space(3)))
; __device__ __forceinline__ float bf_lo(unsigned w) { return __uint_as_float(w << 16); }
; __device__ __forceinline__ float bf_hi(unsigned w) { return __uint_as_float(w & 0xffff0000u); }
; __device__ __forceinline__ void phase_convpool(const Ctx& P, LAS unsigned char* lds, int vcu, int G) {
;     ...
;             for (int q = 0; q < 62; ++q) { const int j = t0 - 15 + q; unsigned w = 0u; if (j >= 0 && j < L) w = *(const unsigned*)(Z + (size_t)(rowbase + j) * 1024 + c0); zr[q] = (f32x2){bf_lo(w), bf_hi(w)}; }
; #pragma unroll
;             for (int tt = 0; tt < 32; ++tt) { f32x2 a = cb;
; #pragma unroll
;                 for (int k = 0; k < 31; ++k) a += wk[k] * zr[tt + k];
;                 *(LAS f32x2*)(tile + tt * 1024 + c0) = a; }
	v_pk_fma_f32 v[218:219], v[46:47], v[158:159], v[218:219]
	v_lshlrev_b32_e32 v154, 16, v155
	v_and_b32_e32 v155, 0xffff0000, v155
	v_pk_fma_f32 v[210:211], v[48:49], v[158:159], v[210:211]
	v_pk_fma_f32 v[218:219], v[48:49], v[156:157], v[218:219]
	v_lshlrev_b32_e32 v152, 16, v153
	v_and_b32_e32 v153, 0xffff0000, v153
	v_pk_fma_f32 v[210:211], v[50:51], v[156:157], v[210:211]
	v_pk_fma_f32 v[218:219], v[50:51], v[154:155], v[218:219]
	v_lshlrev_b32_e32 v150, 16, v151
	v_and_b32_e32 v151, 0xffff0000, v151
	v_pk_fma_f32 v[210:211], v[52:53], v[154:155], v[210:211]
	v_pk_fma_f32 v[218:219], v[52:53], v[152:153], v[218:219]
	v_lshlrev_b32_e32 v148, 16, v149
	v_and_b32_e32 v149, 0xffff0000, v149
	v_pk_fma_f32 v[210:211], v[54:55], v[152:153], v[210:211]
	v_pk_fma_f32 v[218:219], v[54:55], v[150:151], v[218:219]
	v_lshlrev_b32_e32 v146, 16, v147
	v_and_b32_e32 v147, 0xffff0000, v147
	v_pk_fma_f32 v[210:211], v[56:57], v[150:151], v[210:211]
	v_pk_fma_f32 v[218:219], v[56:57], v[148:149], v[218:219]
	v_lshlrev_b32_e32 v144, 16, v145
	v_and_b32_e32 v145, 0xffff0000, v145
	v_pk_fma_f32 v[210:211], v[58:59], v[148:149], v[210:211]
	v_pk_fma_f32 v[218:219], v[58:59], v[146:147], v[218:219]
	v_lshlrev_b32_e32 v142, 16, v143
	v_and_b32_e32 v143, 0xffff0000, v143
	v_pk_fma_f32 v[210:211], v[60:61], v[146:147], v[210:211]
	v_pk_fma_f32 v[218:219], v[60:61], v[144:145], v[218:219]
	v_lshlrev_b32_e32 v140, 16, v141
	v_and_b32_e32 v141, 0xffff0000, v141
	v_pk_fma_f32 v[210:211], v[62:63], v[144:145], v[210:211]
	v_pk_fma_f32 v[218:219], v[62:63], v[142:143], v[218:219]
	v_lshlrev_b32_e32 v138, 16, v139
	v_and_b32_e32 v139, 0xffff0000, v139
	v_pk_fma_f32 v[210:211], v[64:65], v[142:143], v[210:211]
	v_pk_fma_f32 v[218:219], v[64:65], v[140:141], v[218:219]
	v_lshlrev_b32_e32 v134, 16, v135
	v_and_b32_e32 v135, 0xffff0000, v135
	v_pk_fma_f32 v[210:211], v[66:67], v[140:141], v[210:211]
	v_pk_fma_f32 v[218:219], v[66:67], v[138:139], v[218:219]
	v_pk_fma_f32 v[210:211], v[68:69], v[138:139], v[210:211]
	v_pk_fma_f32 v[218:219], v[68:69], v[134:135], v[218:219]
	ds_write2st64_b64 v1, v[210:211], v[218:219] offset1:8
	v_pk_fma_f32 v[208:209], v[8:9], v[208:209], v[70:71]
	v_pk_fma_f32 v[210:211], v[8:9], v[216:217], v[70:71]
	v_pk_fma_f32 v[208:209], v[10:11], v[216:217], v[208:209]
	v_pk_fma_f32 v[210:211], v[10:11], v[214:215], v[210:211]
	v_pk_fma_f32 v[208:209], v[12:13], v[214:215], v[208:209]
	v_pk_fma_f32 v[210:211], v[12:13], v[212:213], v[210:211]
	v_pk_fma_f32 v[208:209], v[14:15], v[212:213], v[208:209]
	v_pk_fma_f32 v[210:211], v[14:15], v[186:187], v[210:211]
	v_pk_fma_f32 v[208:209], v[16:17], v[186:187], v[208:209]
	v_pk_fma_f32 v[210:211], v[16:17], v[184:185], v[210:211]
	v_pk_fma_f32 v[208:209], v[18:19], v[184:185], v[208:209]
	v_pk_fma_f32 v[210:211], v[18:19], v[182:183], v[210:211]
	v_pk_fma_f32 v[208:209], v[20:21], v[182:183], v[208:209]
	v_pk_fma_f32 v[210:211], v[20:21], v[180:181], v[210:211]
	v_pk_fma_f32 v[208:209], v[22:23], v[180:181], v[208:209]
	v_pk_fma_f32 v[210:211], v[22:23], v[178:179], v[210:211]
	v_pk_fma_f32 v[208:209], v[24:25], v[178:179], v[208:209]
	v_pk_fma_f32 v[210:211], v[24:25], v[176:177], v[210:211]
	v_pk_fma_f32 v[208:209], v[26:27], v[176:177], v[208:209]
	v_pk_fma_f32 v[210:211], v[26:27], v[174:175], v[210:211]
	v_pk_fma_f32 v[208:209], v[28:29], v[174:175], v[208:209]
	v_pk_fma_f32 v[210:211], v[28:29], v[172:173], v[210:211]
	v_pk_fma_f32 v[208:209], v[30:31], v[172:173], v[208:209]
	v_pk_fma_f32 v[210:211], v[30:31], v[170:171], v[210:211]
	v_pk_fma_f32 v[208:209], v[32:33], v[170:171], v[208:209]
	v_pk_fma_f32 v[210:211], v[32:33], v[168:169], v[210:211]
	v_pk_fma_f32 v[208:209], v[34:35], v[168:169], v[208:209]
	v_pk_fma_f32 v[210:211], v[34:35], v[166:167], v[210:211]
	v_pk_fma_f32 v[208:209], v[36:37], v[166:167], v[208:209]
	v_pk_fma_f32 v[210:211], v[36:37], v[164:165], v[210:211]
	v_pk_fma_f32 v[208:209], v[38:39], v[164:165], v[208:209]
	v_pk_fma_f32 v[210:211], v[38:39], v[162:163], v[210:211]
	v_pk_fma_f32 v[208:209], v[40:41], v[162:163], v[208:209]
	v_pk_fma_f32 v[210:211], v[40:41], v[160:161], v[210:211]
	v_pk_fma_f32 v[208:209], v[42:43], v[160:161], v[208:209]
	v_pk_fma_f32 v[210:211], v[42:43], v[158:159], v[210:211]
	v_pk_fma_f32 v[208:209], v[44:45], v[158:159], v[208:209]
	v_pk_fma_f32 v[210:211], v[44:45], v[156:157], v[210:211]
	v_pk_fma_f32 v[208:209], v[46:47], v[156:157], v[208:209]
	v_pk_fma_f32 v[210:211], v[46:47], v[154:155], v[210:211]
	v_pk_fma_f32 v[208:209], v[48:49], v[154:155], v[208:209]
	v_pk_fma_f32 v[210:211], v[48:49], v[152:153], v[210:211]
	v_pk_fma_f32 v[208:209], v[50:51], v[152:153], v[208:209]
	v_pk_fma_f32 v[210:211], v[50:51], v[150:151], v[210:211]
	v_pk_fma_f32 v[208:209], v[52:53], v[150:151], v[208:209]
	v_pk_fma_f32 v[210:211], v[52:53], v[148:149], v[210:211]
	v_pk_fma_f32 v[208:209], v[54:55], v[148:149], v[208:209]
	v_pk_fma_f32 v[210:211], v[54:55], v[146:147], v[210:211]
	v_pk_fma_f32 v[208:209], v[56:57], v[146:147], v[208:209]
	v_pk_fma_f32 v[210:211], v[56:57], v[144:145], v[210:211]
	v_pk_fma_f32 v[208:209], v[58:59], v[144:145], v[208:209]
	v_pk_fma_f32 v[210:211], v[58:59], v[142:143], v[210:211]
	v_pk_fma_f32 v[208:209], v[60:61], v[142:143], v[208:209]
	v_pk_fma_f32 v[210:211], v[60:61], v[140:141], v[210:211]
	v_pk_fma_f32 v[208:209], v[62:63], v[140:141], v[208:209]
	v_pk_fma_f32 v[210:211], v[62:63], v[138:139], v[210:211]
	v_lshlrev_b32_e32 v132, 16, v133
	v_and_b32_e32 v133, 0xffff0000, v133
	v_pk_fma_f32 v[208:209], v[64:65], v[138:139], v[208:209]
	v_pk_fma_f32 v[210:211], v[64:65], v[134:135], v[210:211]
	v_lshlrev_b32_e32 v130, 16, v131
; #define LAS __attribute__((address_space(3)))
; __device__ __forceinline__ float bf_lo(unsigned w) { return __uint_as_float(w << 16); }
; __device__ __forceinline__ float bf_hi(unsigned w) { return __uint_as_float(w & 0xffff0000u); }
; __device__ __forceinline__ void phase_convpool(const Ctx& P, LAS unsigned char* lds, int vcu, int G) {
;     ...
;             for (int q = 0; q < 62; ++q) { const int j = t0 - 15 + q; unsigned w = 0u; if (j >= 0 && j < L) w = *(const unsigned*)(Z + (size_t)(rowbase + j) * 1024 + c0); zr[q] = (f32x2){bf_lo(w), bf_hi(w)}; }
; #pragma unroll
;             for (int tt = 0; tt < 32; ++tt) { f32x2 a = cb;
; #pragma unroll
;                 for (int k = 0; k < 31; ++k) a += wk[k] * zr[tt + k];
;                 *(LAS f32x2*)(tile + tt * 1024 + c0) = a; }
	v_and_b32_e32 v131, 0xffff0000, v131
	v_pk_fma_f32 v[208:209], v[66:67], v[134:135], v[208:209]
	v_pk_fma_f32 v[210:211], v[66:67], v[132:133], v[210:211]
	v_pk_fma_f32 v[208:209], v[68:69], v[132:133], v[208:209]
	v_pk_fma_f32 v[210:211], v[68:69], v[130:131], v[210:211]
	ds_write2st64_b64 v1, v[208:209], v[210:211] offset0:16 offset1:24
	v_pk_fma_f32 v[208:209], v[8:9], v[214:215], v[70:71]
	v_pk_fma_f32 v[210:211], v[8:9], v[212:213], v[70:71]
	v_pk_fma_f32 v[208:209], v[10:11], v[212:213], v[208:209]
	v_pk_fma_f32 v[210:211], v[10:11], v[186:187], v[210:211]
	v_pk_fma_f32 v[208:209], v[12:13], v[186:187], v[208:209]
	v_pk_fma_f32 v[186:187], v[8:9], v[186:187], v[70:71]
	v_pk_fma_f32 v[208:209], v[14:15], v[184:185], v[208:209]
	v_pk_fma_f32 v[210:211], v[12:13], v[184:185], v[210:211]
	v_pk_fma_f32 v[186:187], v[10:11], v[184:185], v[186:187]
	v_pk_fma_f32 v[184:185], v[8:9], v[184:185], v[70:71]
	v_pk_fma_f32 v[208:209], v[16:17], v[182:183], v[208:209]
	v_pk_fma_f32 v[210:211], v[14:15], v[182:183], v[210:211]
	v_pk_fma_f32 v[186:187], v[12:13], v[182:183], v[186:187]
	v_pk_fma_f32 v[184:185], v[10:11], v[182:183], v[184:185]
	v_pk_fma_f32 v[182:183], v[8:9], v[182:183], v[70:71]
	v_pk_fma_f32 v[208:209], v[18:19], v[180:181], v[208:209]
	v_pk_fma_f32 v[210:211], v[16:17], v[180:181], v[210:211]
	v_pk_fma_f32 v[186:187], v[14:15], v[180:181], v[186:187]
	v_pk_fma_f32 v[184:185], v[12:13], v[180:181], v[184:185]
	v_pk_fma_f32 v[182:183], v[10:11], v[180:181], v[182:183]
	v_pk_fma_f32 v[180:181], v[8:9], v[180:181], v[70:71]
	v_pk_fma_f32 v[208:209], v[20:21], v[178:179], v[208:209]
	v_pk_fma_f32 v[210:211], v[18:19], v[178:179], v[210:211]
	v_pk_fma_f32 v[186:187], v[16:17], v[178:179], v[186:187]
	v_pk_fma_f32 v[184:185], v[14:15], v[178:179], v[184:185]
	v_pk_fma_f32 v[182:183], v[12:13], v[178:179], v[182:183]
	v_pk_fma_f32 v[180:181], v[10:11], v[178:179], v[180:181]
	v_pk_fma_f32 v[178:179], v[8:9], v[178:179], v[70:71]
	v_pk_fma_f32 v[208:209], v[22:23], v[176:177], v[208:209]
	v_pk_fma_f32 v[210:211], v[20:21], v[176:177], v[210:211]
	v_pk_fma_f32 v[186:187], v[18:19], v[176:177], v[186:187]
	v_pk_fma_f32 v[184:185], v[16:17], v[176:177], v[184:185]
	v_pk_fma_f32 v[182:183], v[14:15], v[176:177], v[182:183]
	v_pk_fma_f32 v[180:181], v[12:13], v[176:177], v[180:181]
	v_pk_fma_f32 v[178:179], v[10:11], v[176:177], v[178:179]
	v_pk_fma_f32 v[176:177], v[8:9], v[176:177], v[70:71]
	v_pk_fma_f32 v[208:209], v[24:25], v[174:175], v[208:209]
	v_pk_fma_f32 v[210:211], v[22:23], v[174:175], v[210:211]
	v_pk_fma_f32 v[186:187], v[20:21], v[174:175], v[186:187]
	v_pk_fma_f32 v[184:185], v[18:19], v[174:175], v[184:185]
	v_pk_fma_f32 v[182:183], v[16:17], v[174:175], v[182:183]
	v_pk_fma_f32 v[180:181], v[14:15], v[174:175], v[180:181]
	v_pk_fma_f32 v[178:179], v[12:13], v[174:175], v[178:179]
	v_pk_fma_f32 v[176:177], v[10:11], v[174:175], v[176:177]
	v_pk_fma_f32 v[174:175], v[8:9], v[174:175], v[70:71]
	v_pk_fma_f32 v[208:209], v[26:27], v[172:173], v[208:209]
	v_pk_fma_f32 v[210:211], v[24:25], v[172:173], v[210:211]
	v_pk_fma_f32 v[186:187], v[22:23], v[172:173], v[186:187]
	v_pk_fma_f32 v[184:185], v[20:21], v[172:173], v[184:185]
	v_pk_fma_f32 v[182:183], v[18:19], v[172:173], v[182:183]
	v_pk_fma_f32 v[180:181], v[16:17], v[172:173], v[180:181]
	v_pk_fma_f32 v[178:179], v[14:15], v[172:173], v[178:179]
	v_pk_fma_f32 v[176:177], v[12:13], v[172:173], v[176:177]
	v_pk_fma_f32 v[174:175], v[10:11], v[172:173], v[174:175]
	v_pk_fma_f32 v[172:173], v[8:9], v[172:173], v[70:71]
	v_pk_fma_f32 v[208:209], v[28:29], v[170:171], v[208:209]
	v_pk_fma_f32 v[210:211], v[26:27], v[170:171], v[210:211]
	v_pk_fma_f32 v[186:187], v[24:25], v[170:171], v[186:187]
	v_pk_fma_f32 v[184:185], v[22:23], v[170:171], v[184:185]
	v_pk_fma_f32 v[182:183], v[20:21], v[170:171], v[182:183]
	v_pk_fma_f32 v[180:181], v[18:19], v[170:171], v[180:181]
	v_pk_fma_f32 v[178:179], v[16:17], v[170:171], v[178:179]
	v_pk_fma_f32 v[176:177], v[14:15], v[170:171], v[176:177]
	v_pk_fma_f32 v[174:175], v[12:13], v[170:171], v[174:175]
	v_pk_fma_f32 v[172:173], v[10:11], v[170:171], v[172:173]
	v_pk_fma_f32 v[170:171], v[8:9], v[170:171], v[70:71]
	v_pk_fma_f32 v[208:209], v[30:31], v[168:169], v[208:209]
	v_pk_fma_f32 v[210:211], v[28:29], v[168:169], v[210:211]
	v_pk_fma_f32 v[186:187], v[26:27], v[168:169], v[186:187]
	v_pk_fma_f32 v[184:185], v[24:25], v[168:169], v[184:185]
	v_pk_fma_f32 v[182:183], v[22:23], v[168:169], v[182:183]
	v_pk_fma_f32 v[180:181], v[20:21], v[168:169], v[180:181]
	v_pk_fma_f32 v[178:179], v[18:19], v[168:169], v[178:179]
	v_pk_fma_f32 v[176:177], v[16:17], v[168:169], v[176:177]
	v_pk_fma_f32 v[174:175], v[14:15], v[168:169], v[174:175]
	v_pk_fma_f32 v[172:173], v[12:13], v[168:169], v[172:173]
	v_pk_fma_f32 v[170:171], v[10:11], v[168:169], v[170:171]
	v_pk_fma_f32 v[168:169], v[8:9], v[168:169], v[70:71]
	v_pk_fma_f32 v[208:209], v[32:33], v[166:167], v[208:209]
	v_pk_fma_f32 v[210:211], v[30:31], v[166:167], v[210:211]
	v_pk_fma_f32 v[186:187], v[28:29], v[166:167], v[186:187]
	v_pk_fma_f32 v[184:185], v[26:27], v[166:167], v[184:185]
	v_pk_fma_f32 v[182:183], v[24:25], v[166:167], v[182:183]
	v_pk_fma_f32 v[180:181], v[22:23], v[166:167], v[180:181]
	v_pk_fma_f32 v[178:179], v[20:21], v[166:167], v[178:179]
	v_pk_fma_f32 v[176:177], v[18:19], v[166:167], v[176:177]
	v_pk_fma_f32 v[174:175], v[16:17], v[166:167], v[174:175]
	v_pk_fma_f32 v[172:173], v[14:15], v[166:167], v[172:173]
	v_pk_fma_f32 v[170:171], v[12:13], v[166:167], v[170:171]
	v_pk_fma_f32 v[168:169], v[10:11], v[166:167], v[168:169]
	v_pk_fma_f32 v[166:167], v[8:9], v[166:167], v[70:71]
; #define LAS __attribute__((address_space(3)))
; __device__ __forceinline__ float bf_lo(unsigned w) { return __uint_as_float(w << 16); }
; __device__ __forceinline__ float bf_hi(unsigned w) { return __uint_as_float(w & 0xffff0000u); }
; __device__ __forceinline__ void phase_convpool(const Ctx& P, LAS unsigned char* lds, int vcu, int G) {
;     ...
;             for (int q = 0; q < 62; ++q) { const int j = t0 - 15 + q; unsigned w = 0u; if (j >= 0 && j < L) w = *(const unsigned*)(Z + (size_t)(rowbase + j) * 1024 + c0); zr[q] = (f32x2){bf_lo(w), bf_hi(w)}; }
; #pragma unroll
;             for (int tt = 0; tt < 32; ++tt) { f32x2 a = cb;
; #pragma unroll
;                 for (int k = 0; k < 31; ++k) a += wk[k] * zr[tt + k];
;                 *(LAS f32x2*)(tile + tt * 1024 + c0) = a; }
	v_pk_fma_f32 v[208:209], v[34:35], v[164:165], v[208:209]
	v_pk_fma_f32 v[210:211], v[32:33], v[164:165], v[210:211]
	v_pk_fma_f32 v[186:187], v[30:31], v[164:165], v[186:187]
	v_pk_fma_f32 v[184:185], v[28:29], v[164:165], v[184:185]
	v_pk_fma_f32 v[182:183], v[26:27], v[164:165], v[182:183]
	v_pk_fma_f32 v[180:181], v[24:25], v[164:165], v[180:181]
	v_pk_fma_f32 v[178:179], v[22:23], v[164:165], v[178:179]
	v_pk_fma_f32 v[176:177], v[20:21], v[164:165], v[176:177]
	v_pk_fma_f32 v[174:175], v[18:19], v[164:165], v[174:175]
	v_pk_fma_f32 v[172:173], v[16:17], v[164:165], v[172:173]
	v_pk_fma_f32 v[170:171], v[14:15], v[164:165], v[170:171]
	v_pk_fma_f32 v[168:169], v[12:13], v[164:165], v[168:169]
	v_pk_fma_f32 v[166:167], v[10:11], v[164:165], v[166:167]
	v_pk_fma_f32 v[164:165], v[8:9], v[164:165], v[70:71]
	v_pk_fma_f32 v[208:209], v[36:37], v[162:163], v[208:209]
	v_pk_fma_f32 v[210:211], v[34:35], v[162:163], v[210:211]
	v_pk_fma_f32 v[186:187], v[32:33], v[162:163], v[186:187]
	v_pk_fma_f32 v[184:185], v[30:31], v[162:163], v[184:185]
	v_pk_fma_f32 v[182:183], v[28:29], v[162:163], v[182:183]
	v_pk_fma_f32 v[180:181], v[26:27], v[162:163], v[180:181]
	v_pk_fma_f32 v[178:179], v[24:25], v[162:163], v[178:179]
	v_pk_fma_f32 v[176:177], v[22:23], v[162:163], v[176:177]
	v_pk_fma_f32 v[174:175], v[20:21], v[162:163], v[174:175]
	v_pk_fma_f32 v[172:173], v[18:19], v[162:163], v[172:173]
	v_pk_fma_f32 v[170:171], v[16:17], v[162:163], v[170:171]
	v_pk_fma_f32 v[168:169], v[14:15], v[162:163], v[168:169]
	v_pk_fma_f32 v[166:167], v[12:13], v[162:163], v[166:167]
	v_pk_fma_f32 v[164:165], v[10:11], v[162:163], v[164:165]
	v_pk_fma_f32 v[162:163], v[8:9], v[162:163], v[70:71]
	v_pk_fma_f32 v[208:209], v[38:39], v[160:161], v[208:209]
	v_pk_fma_f32 v[210:211], v[36:37], v[160:161], v[210:211]
	v_pk_fma_f32 v[186:187], v[34:35], v[160:161], v[186:187]
	v_pk_fma_f32 v[184:185], v[32:33], v[160:161], v[184:185]
	v_pk_fma_f32 v[182:183], v[30:31], v[160:161], v[182:183]
	v_pk_fma_f32 v[180:181], v[28:29], v[160:161], v[180:181]
	v_pk_fma_f32 v[178:179], v[26:27], v[160:161], v[178:179]
	v_pk_fma_f32 v[176:177], v[24:25], v[160:161], v[176:177]
	v_pk_fma_f32 v[174:175], v[22:23], v[160:161], v[174:175]
	v_pk_fma_f32 v[172:173], v[20:21], v[160:161], v[172:173]
	v_pk_fma_f32 v[170:171], v[18:19], v[160:161], v[170:171]
	v_pk_fma_f32 v[168:169], v[16:17], v[160:161], v[168:169]
	v_pk_fma_f32 v[166:167], v[14:15], v[160:161], v[166:167]
	v_pk_fma_f32 v[164:165], v[12:13], v[160:161], v[164:165]
	v_pk_fma_f32 v[162:163], v[10:11], v[160:161], v[162:163]
	v_pk_fma_f32 v[160:161], v[8:9], v[160:161], v[70:71]
	v_pk_fma_f32 v[208:209], v[40:41], v[158:159], v[208:209]
	v_pk_fma_f32 v[210:211], v[38:39], v[158:159], v[210:211]
	v_pk_fma_f32 v[186:187], v[36:37], v[158:159], v[186:187]
	v_pk_fma_f32 v[184:185], v[34:35], v[158:159], v[184:185]
	v_pk_fma_f32 v[182:183], v[32:33], v[158:159], v[182:183]
	v_pk_fma_f32 v[180:181], v[30:31], v[158:159], v[180:181]
	v_pk_fma_f32 v[178:179], v[28:29], v[158:159], v[178:179]
	v_pk_fma_f32 v[176:177], v[26:27], v[158:159], v[176:177]
	v_pk_fma_f32 v[174:175], v[24:25], v[158:159], v[174:175]
	v_pk_fma_f32 v[172:173], v[22:23], v[158:159], v[172:173]
	v_pk_fma_f32 v[170:171], v[20:21], v[158:159], v[170:171]
	v_pk_fma_f32 v[168:169], v[18:19], v[158:159], v[168:169]
	v_pk_fma_f32 v[166:167], v[16:17], v[158:159], v[166:167]
	v_pk_fma_f32 v[164:165], v[14:15], v[158:159], v[164:165]
	v_pk_fma_f32 v[162:163], v[12:13], v[158:159], v[162:163]
	v_pk_fma_f32 v[160:161], v[10:11], v[158:159], v[160:161]
	v_pk_fma_f32 v[158:159], v[8:9], v[158:159], v[70:71]
	v_pk_fma_f32 v[208:209], v[42:43], v[156:157], v[208:209]
	v_pk_fma_f32 v[210:211], v[40:41], v[156:157], v[210:211]
	v_pk_fma_f32 v[186:187], v[38:39], v[156:157], v[186:187]
	v_pk_fma_f32 v[184:185], v[36:37], v[156:157], v[184:185]
	v_pk_fma_f32 v[182:183], v[34:35], v[156:157], v[182:183]
	v_pk_fma_f32 v[180:181], v[32:33], v[156:157], v[180:181]
	v_pk_fma_f32 v[178:179], v[30:31], v[156:157], v[178:179]
	v_pk_fma_f32 v[176:177], v[28:29], v[156:157], v[176:177]
	v_pk_fma_f32 v[174:175], v[26:27], v[156:157], v[174:175]
	v_pk_fma_f32 v[172:173], v[24:25], v[156:157], v[172:173]
	v_pk_fma_f32 v[170:171], v[22:23], v[156:157], v[170:171]
	v_pk_fma_f32 v[168:169], v[20:21], v[156:157], v[168:169]
	v_pk_fma_f32 v[166:167], v[18:19], v[156:157], v[166:167]
	v_pk_fma_f32 v[164:165], v[16:17], v[156:157], v[164:165]
	v_pk_fma_f32 v[162:163], v[14:15], v[156:157], v[162:163]
	v_pk_fma_f32 v[160:161], v[12:13], v[156:157], v[160:161]
	v_pk_fma_f32 v[158:159], v[10:11], v[156:157], v[158:159]
	v_pk_fma_f32 v[156:157], v[8:9], v[156:157], v[70:71]
	v_pk_fma_f32 v[208:209], v[44:45], v[154:155], v[208:209]
	v_pk_fma_f32 v[210:211], v[42:43], v[154:155], v[210:211]
	v_pk_fma_f32 v[186:187], v[40:41], v[154:155], v[186:187]
	v_pk_fma_f32 v[184:185], v[38:39], v[154:155], v[184:185]
	v_pk_fma_f32 v[182:183], v[36:37], v[154:155], v[182:183]
	v_pk_fma_f32 v[180:181], v[34:35], v[154:155], v[180:181]
	v_pk_fma_f32 v[178:179], v[32:33], v[154:155], v[178:179]
	v_pk_fma_f32 v[176:177], v[30:31], v[154:155], v[176:177]
	v_pk_fma_f32 v[174:175], v[28:29], v[154:155], v[174:175]
	v_pk_fma_f32 v[172:173], v[26:27], v[154:155], v[172:173]
	v_pk_fma_f32 v[170:171], v[24:25], v[154:155], v[170:171]
	v_pk_fma_f32 v[168:169], v[22:23], v[154:155], v[168:169]
	v_pk_fma_f32 v[166:167], v[20:21], v[154:155], v[166:167]
	v_pk_fma_f32 v[164:165], v[18:19], v[154:155], v[164:165]
	v_pk_fma_f32 v[162:163], v[16:17], v[154:155], v[162:163]
	v_pk_fma_f32 v[160:161], v[14:15], v[154:155], v[160:161]
; #define LAS __attribute__((address_space(3)))
; __device__ __forceinline__ float bf_lo(unsigned w) { return __uint_as_float(w << 16); }
; __device__ __forceinline__ float bf_hi(unsigned w) { return __uint_as_float(w & 0xffff0000u); }
; __device__ __forceinline__ void phase_convpool(const Ctx& P, LAS unsigned char* lds, int vcu, int G) {
;     ...
;             for (int q = 0; q < 62; ++q) { const int j = t0 - 15 + q; unsigned w = 0u; if (j >= 0 && j < L) w = *(const unsigned*)(Z + (size_t)(rowbase + j) * 1024 + c0); zr[q] = (f32x2){bf_lo(w), bf_hi(w)}; }
; #pragma unroll
;             for (int tt = 0; tt < 32; ++tt) { f32x2 a = cb;
; #pragma unroll
;                 for (int k = 0; k < 31; ++k) a += wk[k] * zr[tt + k];
;                 *(LAS f32x2*)(tile + tt * 1024 + c0) = a; }
	v_pk_fma_f32 v[158:159], v[12:13], v[154:155], v[158:159]
	v_pk_fma_f32 v[156:157], v[10:11], v[154:155], v[156:157]
	v_pk_fma_f32 v[154:155], v[8:9], v[154:155], v[70:71]
	v_pk_fma_f32 v[208:209], v[46:47], v[152:153], v[208:209]
	v_pk_fma_f32 v[210:211], v[44:45], v[152:153], v[210:211]
	v_pk_fma_f32 v[186:187], v[42:43], v[152:153], v[186:187]
	v_pk_fma_f32 v[184:185], v[40:41], v[152:153], v[184:185]
	v_pk_fma_f32 v[182:183], v[38:39], v[152:153], v[182:183]
	v_pk_fma_f32 v[180:181], v[36:37], v[152:153], v[180:181]
	v_pk_fma_f32 v[178:179], v[34:35], v[152:153], v[178:179]
	v_pk_fma_f32 v[176:177], v[32:33], v[152:153], v[176:177]
	v_pk_fma_f32 v[174:175], v[30:31], v[152:153], v[174:175]
	v_pk_fma_f32 v[172:173], v[28:29], v[152:153], v[172:173]
	v_pk_fma_f32 v[170:171], v[26:27], v[152:153], v[170:171]
	v_pk_fma_f32 v[168:169], v[24:25], v[152:153], v[168:169]
	v_pk_fma_f32 v[166:167], v[22:23], v[152:153], v[166:167]
	v_pk_fma_f32 v[164:165], v[20:21], v[152:153], v[164:165]
	v_pk_fma_f32 v[162:163], v[18:19], v[152:153], v[162:163]
	v_pk_fma_f32 v[160:161], v[16:17], v[152:153], v[160:161]
	v_pk_fma_f32 v[158:159], v[14:15], v[152:153], v[158:159]
	v_pk_fma_f32 v[156:157], v[12:13], v[152:153], v[156:157]
	v_pk_fma_f32 v[154:155], v[10:11], v[152:153], v[154:155]
	v_pk_fma_f32 v[152:153], v[8:9], v[152:153], v[70:71]
	v_pk_fma_f32 v[208:209], v[48:49], v[150:151], v[208:209]
	v_pk_fma_f32 v[210:211], v[46:47], v[150:151], v[210:211]
	v_pk_fma_f32 v[186:187], v[44:45], v[150:151], v[186:187]
	v_pk_fma_f32 v[184:185], v[42:43], v[150:151], v[184:185]
	v_pk_fma_f32 v[182:183], v[40:41], v[150:151], v[182:183]
	v_pk_fma_f32 v[180:181], v[38:39], v[150:151], v[180:181]
	v_pk_fma_f32 v[178:179], v[36:37], v[150:151], v[178:179]
	v_pk_fma_f32 v[176:177], v[34:35], v[150:151], v[176:177]
	v_pk_fma_f32 v[174:175], v[32:33], v[150:151], v[174:175]
	v_pk_fma_f32 v[172:173], v[30:31], v[150:151], v[172:173]
	v_pk_fma_f32 v[170:171], v[28:29], v[150:151], v[170:171]
	v_pk_fma_f32 v[168:169], v[26:27], v[150:151], v[168:169]
	v_pk_fma_f32 v[166:167], v[24:25], v[150:151], v[166:167]
	v_pk_fma_f32 v[164:165], v[22:23], v[150:151], v[164:165]
	v_pk_fma_f32 v[162:163], v[20:21], v[150:151], v[162:163]
	v_pk_fma_f32 v[160:161], v[18:19], v[150:151], v[160:161]
	v_pk_fma_f32 v[158:159], v[16:17], v[150:151], v[158:159]
	v_pk_fma_f32 v[156:157], v[14:15], v[150:151], v[156:157]
	v_pk_fma_f32 v[154:155], v[12:13], v[150:151], v[154:155]
	v_pk_fma_f32 v[152:153], v[10:11], v[150:151], v[152:153]
	v_pk_fma_f32 v[150:151], v[8:9], v[150:151], v[70:71]
	v_pk_fma_f32 v[208:209], v[50:51], v[148:149], v[208:209]
	v_pk_fma_f32 v[210:211], v[48:49], v[148:149], v[210:211]
	v_pk_fma_f32 v[186:187], v[46:47], v[148:149], v[186:187]
	v_pk_fma_f32 v[184:185], v[44:45], v[148:149], v[184:185]
	v_pk_fma_f32 v[182:183], v[42:43], v[148:149], v[182:183]
	v_pk_fma_f32 v[180:181], v[40:41], v[148:149], v[180:181]
	v_pk_fma_f32 v[178:179], v[38:39], v[148:149], v[178:179]
	v_pk_fma_f32 v[176:177], v[36:37], v[148:149], v[176:177]
	v_pk_fma_f32 v[174:175], v[34:35], v[148:149], v[174:175]
	v_pk_fma_f32 v[172:173], v[32:33], v[148:149], v[172:173]
	v_pk_fma_f32 v[170:171], v[30:31], v[148:149], v[170:171]
	v_pk_fma_f32 v[168:169], v[28:29], v[148:149], v[168:169]
	v_pk_fma_f32 v[166:167], v[26:27], v[148:149], v[166:167]
	v_pk_fma_f32 v[164:165], v[24:25], v[148:149], v[164:165]
	v_pk_fma_f32 v[162:163], v[22:23], v[148:149], v[162:163]
	v_pk_fma_f32 v[160:161], v[20:21], v[148:149], v[160:161]
	v_pk_fma_f32 v[158:159], v[18:19], v[148:149], v[158:159]
	v_pk_fma_f32 v[156:157], v[16:17], v[148:149], v[156:157]
	v_pk_fma_f32 v[154:155], v[14:15], v[148:149], v[154:155]
	v_pk_fma_f32 v[152:153], v[12:13], v[148:149], v[152:153]
	v_pk_fma_f32 v[150:151], v[10:11], v[148:149], v[150:151]
	v_pk_fma_f32 v[148:149], v[8:9], v[148:149], v[70:71]
	v_pk_fma_f32 v[208:209], v[52:53], v[146:147], v[208:209]
	v_pk_fma_f32 v[210:211], v[50:51], v[146:147], v[210:211]
	v_pk_fma_f32 v[186:187], v[48:49], v[146:147], v[186:187]
	v_pk_fma_f32 v[184:185], v[46:47], v[146:147], v[184:185]
	v_pk_fma_f32 v[182:183], v[44:45], v[146:147], v[182:183]
	v_pk_fma_f32 v[180:181], v[42:43], v[146:147], v[180:181]
	v_pk_fma_f32 v[178:179], v[40:41], v[146:147], v[178:179]
	v_pk_fma_f32 v[176:177], v[38:39], v[146:147], v[176:177]
	v_pk_fma_f32 v[174:175], v[36:37], v[146:147], v[174:175]
	v_pk_fma_f32 v[172:173], v[34:35], v[146:147], v[172:173]
	v_pk_fma_f32 v[170:171], v[32:33], v[146:147], v[170:171]
	v_pk_fma_f32 v[168:169], v[30:31], v[146:147], v[168:169]
	v_pk_fma_f32 v[166:167], v[28:29], v[146:147], v[166:167]
	v_pk_fma_f32 v[164:165], v[26:27], v[146:147], v[164:165]
	v_pk_fma_f32 v[162:163], v[24:25], v[146:147], v[162:163]
	v_pk_fma_f32 v[160:161], v[22:23], v[146:147], v[160:161]
	v_pk_fma_f32 v[158:159], v[20:21], v[146:147], v[158:159]
	v_pk_fma_f32 v[156:157], v[18:19], v[146:147], v[156:157]
	v_pk_fma_f32 v[154:155], v[16:17], v[146:147], v[154:155]
	v_pk_fma_f32 v[152:153], v[14:15], v[146:147], v[152:153]
	v_pk_fma_f32 v[150:151], v[12:13], v[146:147], v[150:151]
	v_pk_fma_f32 v[148:149], v[10:11], v[146:147], v[148:149]
	v_pk_fma_f32 v[146:147], v[8:9], v[146:147], v[70:71]
	v_pk_fma_f32 v[208:209], v[54:55], v[144:145], v[208:209]
	v_pk_fma_f32 v[210:211], v[52:53], v[144:145], v[210:211]
	v_pk_fma_f32 v[186:187], v[50:51], v[144:145], v[186:187]
	v_pk_fma_f32 v[184:185], v[48:49], v[144:145], v[184:185]
	v_pk_fma_f32 v[182:183], v[46:47], v[144:145], v[182:183]
	v_pk_fma_f32 v[180:181], v[44:45], v[144:145], v[180:181]
	v_pk_fma_f32 v[178:179], v[42:43], v[144:145], v[178:179]
; #define LAS __attribute__((address_space(3)))
; __device__ __forceinline__ float bf_lo(unsigned w) { return __uint_as_float(w << 16); }
; __device__ __forceinline__ float bf_hi(unsigned w) { return __uint_as_float(w & 0xffff0000u); }
; __device__ __forceinline__ void phase_convpool(const Ctx& P, LAS unsigned char* lds, int vcu, int G) {
;     ...
;             for (int q = 0; q < 62; ++q) { const int j = t0 - 15 + q; unsigned w = 0u; if (j >= 0 && j < L) w = *(const unsigned*)(Z + (size_t)(rowbase + j) * 1024 + c0); zr[q] = (f32x2){bf_lo(w), bf_hi(w)}; }
; #pragma unroll
;             for (int tt = 0; tt < 32; ++tt) { f32x2 a = cb;
; #pragma unroll
;                 for (int k = 0; k < 31; ++k) a += wk[k] * zr[tt + k];
;                 *(LAS f32x2*)(tile + tt * 1024 + c0) = a; }
	v_pk_fma_f32 v[176:177], v[40:41], v[144:145], v[176:177]
	v_pk_fma_f32 v[174:175], v[38:39], v[144:145], v[174:175]
	v_pk_fma_f32 v[172:173], v[36:37], v[144:145], v[172:173]
	v_pk_fma_f32 v[170:171], v[34:35], v[144:145], v[170:171]
	v_pk_fma_f32 v[168:169], v[32:33], v[144:145], v[168:169]
	v_pk_fma_f32 v[166:167], v[30:31], v[144:145], v[166:167]
	v_pk_fma_f32 v[164:165], v[28:29], v[144:145], v[164:165]
	v_pk_fma_f32 v[162:163], v[26:27], v[144:145], v[162:163]
	v_pk_fma_f32 v[160:161], v[24:25], v[144:145], v[160:161]
	v_pk_fma_f32 v[158:159], v[22:23], v[144:145], v[158:159]
	v_pk_fma_f32 v[156:157], v[20:21], v[144:145], v[156:157]
	v_pk_fma_f32 v[154:155], v[18:19], v[144:145], v[154:155]
	v_pk_fma_f32 v[152:153], v[16:17], v[144:145], v[152:153]
	v_pk_fma_f32 v[150:151], v[14:15], v[144:145], v[150:151]
	v_pk_fma_f32 v[148:149], v[12:13], v[144:145], v[148:149]
	v_pk_fma_f32 v[146:147], v[10:11], v[144:145], v[146:147]
	v_pk_fma_f32 v[144:145], v[8:9], v[144:145], v[70:71]
	v_pk_fma_f32 v[208:209], v[56:57], v[142:143], v[208:209]
	v_pk_fma_f32 v[210:211], v[54:55], v[142:143], v[210:211]
	v_pk_fma_f32 v[186:187], v[52:53], v[142:143], v[186:187]
	v_pk_fma_f32 v[184:185], v[50:51], v[142:143], v[184:185]
	v_pk_fma_f32 v[182:183], v[48:49], v[142:143], v[182:183]
	v_pk_fma_f32 v[180:181], v[46:47], v[142:143], v[180:181]
	v_pk_fma_f32 v[178:179], v[44:45], v[142:143], v[178:179]
	v_pk_fma_f32 v[176:177], v[42:43], v[142:143], v[176:177]
	v_pk_fma_f32 v[174:175], v[40:41], v[142:143], v[174:175]
	v_pk_fma_f32 v[172:173], v[38:39], v[142:143], v[172:173]
	v_pk_fma_f32 v[170:171], v[36:37], v[142:143], v[170:171]
	v_pk_fma_f32 v[168:169], v[34:35], v[142:143], v[168:169]
	v_pk_fma_f32 v[166:167], v[32:33], v[142:143], v[166:167]
	v_pk_fma_f32 v[164:165], v[30:31], v[142:143], v[164:165]
	v_pk_fma_f32 v[162:163], v[28:29], v[142:143], v[162:163]
	v_pk_fma_f32 v[160:161], v[26:27], v[142:143], v[160:161]
	v_pk_fma_f32 v[158:159], v[24:25], v[142:143], v[158:159]
	v_pk_fma_f32 v[156:157], v[22:23], v[142:143], v[156:157]
	v_pk_fma_f32 v[154:155], v[20:21], v[142:143], v[154:155]
	v_pk_fma_f32 v[152:153], v[18:19], v[142:143], v[152:153]
	v_pk_fma_f32 v[150:151], v[16:17], v[142:143], v[150:151]
	v_pk_fma_f32 v[148:149], v[14:15], v[142:143], v[148:149]
	v_pk_fma_f32 v[146:147], v[12:13], v[142:143], v[146:147]
	v_pk_fma_f32 v[144:145], v[10:11], v[142:143], v[144:145]
	v_pk_fma_f32 v[142:143], v[8:9], v[142:143], v[70:71]
	v_pk_fma_f32 v[208:209], v[58:59], v[140:141], v[208:209]
	v_pk_fma_f32 v[210:211], v[56:57], v[140:141], v[210:211]
	v_pk_fma_f32 v[186:187], v[54:55], v[140:141], v[186:187]
	v_pk_fma_f32 v[184:185], v[52:53], v[140:141], v[184:185]
	v_pk_fma_f32 v[182:183], v[50:51], v[140:141], v[182:183]
	v_pk_fma_f32 v[180:181], v[48:49], v[140:141], v[180:181]
	v_pk_fma_f32 v[178:179], v[46:47], v[140:141], v[178:179]
	v_pk_fma_f32 v[176:177], v[44:45], v[140:141], v[176:177]
	v_pk_fma_f32 v[174:175], v[42:43], v[140:141], v[174:175]
	v_pk_fma_f32 v[172:173], v[40:41], v[140:141], v[172:173]
	v_pk_fma_f32 v[170:171], v[38:39], v[140:141], v[170:171]
	v_pk_fma_f32 v[168:169], v[36:37], v[140:141], v[168:169]
	v_pk_fma_f32 v[166:167], v[34:35], v[140:141], v[166:167]
	v_pk_fma_f32 v[164:165], v[32:33], v[140:141], v[164:165]
	v_pk_fma_f32 v[162:163], v[30:31], v[140:141], v[162:163]
	v_pk_fma_f32 v[160:161], v[28:29], v[140:141], v[160:161]
	v_pk_fma_f32 v[158:159], v[26:27], v[140:141], v[158:159]
	v_pk_fma_f32 v[156:157], v[24:25], v[140:141], v[156:157]
	v_pk_fma_f32 v[154:155], v[22:23], v[140:141], v[154:155]
	v_pk_fma_f32 v[152:153], v[20:21], v[140:141], v[152:153]
	v_pk_fma_f32 v[150:151], v[18:19], v[140:141], v[150:151]
	v_pk_fma_f32 v[148:149], v[16:17], v[140:141], v[148:149]
	v_pk_fma_f32 v[146:147], v[14:15], v[140:141], v[146:147]
	v_pk_fma_f32 v[144:145], v[12:13], v[140:141], v[144:145]
	v_pk_fma_f32 v[142:143], v[10:11], v[140:141], v[142:143]
	v_pk_fma_f32 v[140:141], v[8:9], v[140:141], v[70:71]
	v_pk_fma_f32 v[208:209], v[60:61], v[138:139], v[208:209]
	v_pk_fma_f32 v[210:211], v[58:59], v[138:139], v[210:211]
	v_pk_fma_f32 v[186:187], v[56:57], v[138:139], v[186:187]
	v_pk_fma_f32 v[184:185], v[54:55], v[138:139], v[184:185]
	v_pk_fma_f32 v[182:183], v[52:53], v[138:139], v[182:183]
	v_pk_fma_f32 v[180:181], v[50:51], v[138:139], v[180:181]
	v_pk_fma_f32 v[178:179], v[48:49], v[138:139], v[178:179]
	v_pk_fma_f32 v[176:177], v[46:47], v[138:139], v[176:177]
	v_pk_fma_f32 v[174:175], v[44:45], v[138:139], v[174:175]
	v_pk_fma_f32 v[172:173], v[42:43], v[138:139], v[172:173]
	v_pk_fma_f32 v[170:171], v[40:41], v[138:139], v[170:171]
	v_pk_fma_f32 v[168:169], v[38:39], v[138:139], v[168:169]
	v_pk_fma_f32 v[166:167], v[36:37], v[138:139], v[166:167]
	v_pk_fma_f32 v[164:165], v[34:35], v[138:139], v[164:165]
	v_pk_fma_f32 v[162:163], v[32:33], v[138:139], v[162:163]
	v_pk_fma_f32 v[160:161], v[30:31], v[138:139], v[160:161]
	v_pk_fma_f32 v[158:159], v[28:29], v[138:139], v[158:159]
	v_pk_fma_f32 v[156:157], v[26:27], v[138:139], v[156:157]
	v_pk_fma_f32 v[154:155], v[24:25], v[138:139], v[154:155]
	v_pk_fma_f32 v[152:153], v[22:23], v[138:139], v[152:153]
	v_pk_fma_f32 v[150:151], v[20:21], v[138:139], v[150:151]
	v_pk_fma_f32 v[148:149], v[18:19], v[138:139], v[148:149]
	v_pk_fma_f32 v[146:147], v[16:17], v[138:139], v[146:147]
	v_pk_fma_f32 v[144:145], v[14:15], v[138:139], v[144:145]
	v_pk_fma_f32 v[142:143], v[12:13], v[138:139], v[142:143]
	v_pk_fma_f32 v[140:141], v[10:11], v[138:139], v[140:141]
	v_pk_fma_f32 v[138:139], v[8:9], v[138:139], v[70:71]
	v_pk_fma_f32 v[208:209], v[62:63], v[134:135], v[208:209]
; #define LAS __attribute__((address_space(3)))
; __device__ __forceinline__ float bf_lo(unsigned w) { return __uint_as_float(w << 16); }
; __device__ __forceinline__ float bf_hi(unsigned w) { return __uint_as_float(w & 0xffff0000u); }
; __device__ __forceinline__ void phase_convpool(const Ctx& P, LAS unsigned char* lds, int vcu, int G) {
;     ...
;             for (int q = 0; q < 62; ++q) { const int j = t0 - 15 + q; unsigned w = 0u; if (j >= 0 && j < L) w = *(const unsigned*)(Z + (size_t)(rowbase + j) * 1024 + c0); zr[q] = (f32x2){bf_lo(w), bf_hi(w)}; }
; #pragma unroll
;             for (int tt = 0; tt < 32; ++tt) { f32x2 a = cb;
; #pragma unroll
;                 for (int k = 0; k < 31; ++k) a += wk[k] * zr[tt + k];
;                 *(LAS f32x2*)(tile + tt * 1024 + c0) = a; }
	v_pk_fma_f32 v[210:211], v[60:61], v[134:135], v[210:211]
	v_pk_fma_f32 v[186:187], v[58:59], v[134:135], v[186:187]
	v_pk_fma_f32 v[184:185], v[56:57], v[134:135], v[184:185]
	v_pk_fma_f32 v[182:183], v[54:55], v[134:135], v[182:183]
	v_pk_fma_f32 v[180:181], v[52:53], v[134:135], v[180:181]
	v_pk_fma_f32 v[178:179], v[50:51], v[134:135], v[178:179]
	v_pk_fma_f32 v[176:177], v[48:49], v[134:135], v[176:177]
	v_pk_fma_f32 v[174:175], v[46:47], v[134:135], v[174:175]
	v_pk_fma_f32 v[172:173], v[44:45], v[134:135], v[172:173]
	v_pk_fma_f32 v[170:171], v[42:43], v[134:135], v[170:171]
	v_pk_fma_f32 v[168:169], v[40:41], v[134:135], v[168:169]
	v_pk_fma_f32 v[166:167], v[38:39], v[134:135], v[166:167]
	v_pk_fma_f32 v[164:165], v[36:37], v[134:135], v[164:165]
	v_pk_fma_f32 v[162:163], v[34:35], v[134:135], v[162:163]
	v_pk_fma_f32 v[160:161], v[32:33], v[134:135], v[160:161]
	v_pk_fma_f32 v[158:159], v[30:31], v[134:135], v[158:159]
	v_pk_fma_f32 v[156:157], v[28:29], v[134:135], v[156:157]
	v_pk_fma_f32 v[154:155], v[26:27], v[134:135], v[154:155]
	v_pk_fma_f32 v[152:153], v[24:25], v[134:135], v[152:153]
	v_pk_fma_f32 v[150:151], v[22:23], v[134:135], v[150:151]
	v_pk_fma_f32 v[148:149], v[20:21], v[134:135], v[148:149]
	v_pk_fma_f32 v[146:147], v[18:19], v[134:135], v[146:147]
	v_pk_fma_f32 v[144:145], v[16:17], v[134:135], v[144:145]
	v_pk_fma_f32 v[142:143], v[14:15], v[134:135], v[142:143]
	v_pk_fma_f32 v[140:141], v[12:13], v[134:135], v[140:141]
	v_pk_fma_f32 v[138:139], v[10:11], v[134:135], v[138:139]
	v_pk_fma_f32 v[134:135], v[8:9], v[134:135], v[70:71]
	v_pk_fma_f32 v[208:209], v[64:65], v[132:133], v[208:209]
	v_pk_fma_f32 v[210:211], v[62:63], v[132:133], v[210:211]
	v_pk_fma_f32 v[186:187], v[60:61], v[132:133], v[186:187]
	v_pk_fma_f32 v[184:185], v[58:59], v[132:133], v[184:185]
	v_pk_fma_f32 v[182:183], v[56:57], v[132:133], v[182:183]
	v_pk_fma_f32 v[180:181], v[54:55], v[132:133], v[180:181]
	v_pk_fma_f32 v[178:179], v[52:53], v[132:133], v[178:179]
	v_pk_fma_f32 v[176:177], v[50:51], v[132:133], v[176:177]
	v_pk_fma_f32 v[174:175], v[48:49], v[132:133], v[174:175]
	v_pk_fma_f32 v[172:173], v[46:47], v[132:133], v[172:173]
	v_pk_fma_f32 v[170:171], v[44:45], v[132:133], v[170:171]
	v_pk_fma_f32 v[168:169], v[42:43], v[132:133], v[168:169]
	v_pk_fma_f32 v[166:167], v[40:41], v[132:133], v[166:167]
	v_pk_fma_f32 v[164:165], v[38:39], v[132:133], v[164:165]
	v_pk_fma_f32 v[162:163], v[36:37], v[132:133], v[162:163]
	v_pk_fma_f32 v[160:161], v[34:35], v[132:133], v[160:161]
	v_pk_fma_f32 v[158:159], v[32:33], v[132:133], v[158:159]
	v_pk_fma_f32 v[156:157], v[30:31], v[132:133], v[156:157]
	v_pk_fma_f32 v[154:155], v[28:29], v[132:133], v[154:155]
	v_pk_fma_f32 v[152:153], v[26:27], v[132:133], v[152:153]
	v_pk_fma_f32 v[150:151], v[24:25], v[132:133], v[150:151]
	v_pk_fma_f32 v[148:149], v[22:23], v[132:133], v[148:149]
	v_pk_fma_f32 v[146:147], v[20:21], v[132:133], v[146:147]
	v_pk_fma_f32 v[144:145], v[18:19], v[132:133], v[144:145]
	v_pk_fma_f32 v[142:143], v[16:17], v[132:133], v[142:143]
	v_pk_fma_f32 v[140:141], v[14:15], v[132:133], v[140:141]
	v_pk_fma_f32 v[138:139], v[12:13], v[132:133], v[138:139]
	v_pk_fma_f32 v[132:133], v[10:11], v[132:133], v[134:135]
	v_lshlrev_b32_e32 v128, 16, v129
	v_and_b32_e32 v129, 0xffff0000, v129
	v_pk_fma_f32 v[208:209], v[66:67], v[130:131], v[208:209]
	v_pk_fma_f32 v[210:211], v[64:65], v[130:131], v[210:211]
	v_pk_fma_f32 v[186:187], v[62:63], v[130:131], v[186:187]
	v_pk_fma_f32 v[184:185], v[60:61], v[130:131], v[184:185]
	v_pk_fma_f32 v[182:183], v[58:59], v[130:131], v[182:183]
	v_pk_fma_f32 v[180:181], v[56:57], v[130:131], v[180:181]
	v_pk_fma_f32 v[178:179], v[54:55], v[130:131], v[178:179]
	v_pk_fma_f32 v[176:177], v[52:53], v[130:131], v[176:177]
	v_pk_fma_f32 v[174:175], v[50:51], v[130:131], v[174:175]
	v_pk_fma_f32 v[172:173], v[48:49], v[130:131], v[172:173]
	v_pk_fma_f32 v[170:171], v[46:47], v[130:131], v[170:171]
	v_pk_fma_f32 v[168:169], v[44:45], v[130:131], v[168:169]
	v_pk_fma_f32 v[166:167], v[42:43], v[130:131], v[166:167]
	v_pk_fma_f32 v[164:165], v[40:41], v[130:131], v[164:165]
	v_pk_fma_f32 v[162:163], v[38:39], v[130:131], v[162:163]
	v_pk_fma_f32 v[160:161], v[36:37], v[130:131], v[160:161]
	v_pk_fma_f32 v[158:159], v[34:35], v[130:131], v[158:159]
	v_pk_fma_f32 v[156:157], v[32:33], v[130:131], v[156:157]
	v_pk_fma_f32 v[154:155], v[30:31], v[130:131], v[154:155]
	v_pk_fma_f32 v[152:153], v[28:29], v[130:131], v[152:153]
	v_pk_fma_f32 v[150:151], v[26:27], v[130:131], v[150:151]
	v_pk_fma_f32 v[148:149], v[24:25], v[130:131], v[148:149]
	v_pk_fma_f32 v[146:147], v[22:23], v[130:131], v[146:147]
	v_pk_fma_f32 v[144:145], v[20:21], v[130:131], v[144:145]
	v_pk_fma_f32 v[142:143], v[18:19], v[130:131], v[142:143]
	v_pk_fma_f32 v[140:141], v[16:17], v[130:131], v[140:141]
	v_pk_fma_f32 v[138:139], v[14:15], v[130:131], v[138:139]
	v_pk_fma_f32 v[130:131], v[12:13], v[130:131], v[132:133]
	v_lshlrev_b32_e32 v126, 16, v127
	v_and_b32_e32 v127, 0xffff0000, v127
	v_pk_fma_f32 v[208:209], v[68:69], v[128:129], v[208:209]
	v_pk_fma_f32 v[210:211], v[66:67], v[128:129], v[210:211]
	v_pk_fma_f32 v[186:187], v[64:65], v[128:129], v[186:187]
	v_pk_fma_f32 v[184:185], v[62:63], v[128:129], v[184:185]
	v_pk_fma_f32 v[182:183], v[60:61], v[128:129], v[182:183]
	v_pk_fma_f32 v[180:181], v[58:59], v[128:129], v[180:181]
	v_pk_fma_f32 v[178:179], v[56:57], v[128:129], v[178:179]
	v_pk_fma_f32 v[176:177], v[54:55], v[128:129], v[176:177]
	v_pk_fma_f32 v[174:175], v[52:53], v[128:129], v[174:175]
	v_pk_fma_f32 v[172:173], v[50:51], v[128:129], v[172:173]
; #define LAS __attribute__((address_space(3)))
; __device__ __forceinline__ float bf_lo(unsigned w) { return __uint_as_float(w << 16); }
; __device__ __forceinline__ float bf_hi(unsigned w) { return __uint_as_float(w & 0xffff0000u); }
; __device__ __forceinline__ void phase_convpool(const Ctx& P, LAS unsigned char* lds, int vcu, int G) {
;     ...
;             for (int q = 0; q < 62; ++q) { const int j = t0 - 15 + q; unsigned w = 0u; if (j >= 0 && j < L) w = *(const unsigned*)(Z + (size_t)(rowbase + j) * 1024 + c0); zr[q] = (f32x2){bf_lo(w), bf_hi(w)}; }
; #pragma unroll
;             for (int tt = 0; tt < 32; ++tt) { f32x2 a = cb;
; #pragma unroll
;                 for (int k = 0; k < 31; ++k) a += wk[k] * zr[tt + k];
;                 *(LAS f32x2*)(tile + tt * 1024 + c0) = a; }
	v_pk_fma_f32 v[170:171], v[48:49], v[128:129], v[170:171]
	v_pk_fma_f32 v[168:169], v[46:47], v[128:129], v[168:169]
	v_pk_fma_f32 v[166:167], v[44:45], v[128:129], v[166:167]
	v_pk_fma_f32 v[164:165], v[42:43], v[128:129], v[164:165]
	v_pk_fma_f32 v[162:163], v[40:41], v[128:129], v[162:163]
	v_pk_fma_f32 v[160:161], v[38:39], v[128:129], v[160:161]
	v_pk_fma_f32 v[158:159], v[36:37], v[128:129], v[158:159]
	v_pk_fma_f32 v[156:157], v[34:35], v[128:129], v[156:157]
	v_pk_fma_f32 v[154:155], v[32:33], v[128:129], v[154:155]
	v_pk_fma_f32 v[152:153], v[30:31], v[128:129], v[152:153]
	v_pk_fma_f32 v[150:151], v[28:29], v[128:129], v[150:151]
	v_pk_fma_f32 v[148:149], v[26:27], v[128:129], v[148:149]
	v_pk_fma_f32 v[146:147], v[24:25], v[128:129], v[146:147]
	v_pk_fma_f32 v[144:145], v[22:23], v[128:129], v[144:145]
	v_pk_fma_f32 v[142:143], v[20:21], v[128:129], v[142:143]
	v_pk_fma_f32 v[140:141], v[18:19], v[128:129], v[140:141]
	v_pk_fma_f32 v[138:139], v[16:17], v[128:129], v[138:139]
	v_pk_fma_f32 v[128:129], v[14:15], v[128:129], v[130:131]
	v_lshlrev_b32_e32 v124, 16, v125
	v_and_b32_e32 v125, 0xffff0000, v125
	v_pk_fma_f32 v[210:211], v[68:69], v[126:127], v[210:211]
	v_pk_fma_f32 v[186:187], v[66:67], v[126:127], v[186:187]
	v_pk_fma_f32 v[184:185], v[64:65], v[126:127], v[184:185]
	v_pk_fma_f32 v[182:183], v[62:63], v[126:127], v[182:183]
	v_pk_fma_f32 v[180:181], v[60:61], v[126:127], v[180:181]
	v_pk_fma_f32 v[178:179], v[58:59], v[126:127], v[178:179]
	v_pk_fma_f32 v[176:177], v[56:57], v[126:127], v[176:177]
	v_pk_fma_f32 v[174:175], v[54:55], v[126:127], v[174:175]
	v_pk_fma_f32 v[172:173], v[52:53], v[126:127], v[172:173]
	v_pk_fma_f32 v[170:171], v[50:51], v[126:127], v[170:171]
	v_pk_fma_f32 v[168:169], v[48:49], v[126:127], v[168:169]
	v_pk_fma_f32 v[166:167], v[46:47], v[126:127], v[166:167]
	v_pk_fma_f32 v[164:165], v[44:45], v[126:127], v[164:165]
	v_pk_fma_f32 v[162:163], v[42:43], v[126:127], v[162:163]
	v_pk_fma_f32 v[160:161], v[40:41], v[126:127], v[160:161]
	v_pk_fma_f32 v[158:159], v[38:39], v[126:127], v[158:159]
	v_pk_fma_f32 v[156:157], v[36:37], v[126:127], v[156:157]
	v_pk_fma_f32 v[154:155], v[34:35], v[126:127], v[154:155]
	v_pk_fma_f32 v[152:153], v[32:33], v[126:127], v[152:153]
	v_pk_fma_f32 v[150:151], v[30:31], v[126:127], v[150:151]
	v_pk_fma_f32 v[148:149], v[28:29], v[126:127], v[148:149]
	v_pk_fma_f32 v[146:147], v[26:27], v[126:127], v[146:147]
	v_pk_fma_f32 v[144:145], v[24:25], v[126:127], v[144:145]
	v_pk_fma_f32 v[142:143], v[22:23], v[126:127], v[142:143]
	v_pk_fma_f32 v[140:141], v[20:21], v[126:127], v[140:141]
	v_pk_fma_f32 v[138:139], v[18:19], v[126:127], v[138:139]
	v_pk_fma_f32 v[126:127], v[16:17], v[126:127], v[128:129]
	v_lshlrev_b32_e32 v122, 16, v123
	v_and_b32_e32 v123, 0xffff0000, v123
	v_pk_fma_f32 v[186:187], v[68:69], v[124:125], v[186:187]
	v_pk_fma_f32 v[184:185], v[66:67], v[124:125], v[184:185]
	v_pk_fma_f32 v[182:183], v[64:65], v[124:125], v[182:183]
	v_pk_fma_f32 v[180:181], v[62:63], v[124:125], v[180:181]
	v_pk_fma_f32 v[178:179], v[60:61], v[124:125], v[178:179]
	v_pk_fma_f32 v[176:177], v[58:59], v[124:125], v[176:177]
	v_pk_fma_f32 v[174:175], v[56:57], v[124:125], v[174:175]
	v_pk_fma_f32 v[172:173], v[54:55], v[124:125], v[172:173]
	v_pk_fma_f32 v[170:171], v[52:53], v[124:125], v[170:171]
	v_pk_fma_f32 v[168:169], v[50:51], v[124:125], v[168:169]
	v_pk_fma_f32 v[166:167], v[48:49], v[124:125], v[166:167]
	v_pk_fma_f32 v[164:165], v[46:47], v[124:125], v[164:165]
	v_pk_fma_f32 v[162:163], v[44:45], v[124:125], v[162:163]
	v_pk_fma_f32 v[160:161], v[42:43], v[124:125], v[160:161]
	v_pk_fma_f32 v[158:159], v[40:41], v[124:125], v[158:159]
	v_pk_fma_f32 v[156:157], v[38:39], v[124:125], v[156:157]
	v_pk_fma_f32 v[154:155], v[36:37], v[124:125], v[154:155]
	v_pk_fma_f32 v[152:153], v[34:35], v[124:125], v[152:153]
	v_pk_fma_f32 v[150:151], v[32:33], v[124:125], v[150:151]
	v_pk_fma_f32 v[148:149], v[30:31], v[124:125], v[148:149]
	v_pk_fma_f32 v[146:147], v[28:29], v[124:125], v[146:147]
	v_pk_fma_f32 v[144:145], v[26:27], v[124:125], v[144:145]
	v_pk_fma_f32 v[142:143], v[24:25], v[124:125], v[142:143]
	v_pk_fma_f32 v[140:141], v[22:23], v[124:125], v[140:141]
	v_pk_fma_f32 v[138:139], v[20:21], v[124:125], v[138:139]
	v_pk_fma_f32 v[124:125], v[18:19], v[124:125], v[126:127]
	v_lshlrev_b32_e32 v120, 16, v121
	v_and_b32_e32 v121, 0xffff0000, v121
	v_pk_fma_f32 v[184:185], v[68:69], v[122:123], v[184:185]
	v_pk_fma_f32 v[182:183], v[66:67], v[122:123], v[182:183]
	v_pk_fma_f32 v[180:181], v[64:65], v[122:123], v[180:181]
	v_pk_fma_f32 v[178:179], v[62:63], v[122:123], v[178:179]
	v_pk_fma_f32 v[176:177], v[60:61], v[122:123], v[176:177]
	v_pk_fma_f32 v[174:175], v[58:59], v[122:123], v[174:175]
	v_pk_fma_f32 v[172:173], v[56:57], v[122:123], v[172:173]
	v_pk_fma_f32 v[170:171], v[54:55], v[122:123], v[170:171]
	v_pk_fma_f32 v[168:169], v[52:53], v[122:123], v[168:169]
	v_pk_fma_f32 v[166:167], v[50:51], v[122:123], v[166:167]
	v_pk_fma_f32 v[164:165], v[48:49], v[122:123], v[164:165]
	v_pk_fma_f32 v[162:163], v[46:47], v[122:123], v[162:163]
	v_pk_fma_f32 v[160:161], v[44:45], v[122:123], v[160:161]
	v_pk_fma_f32 v[158:159], v[42:43], v[122:123], v[158:159]
	v_pk_fma_f32 v[156:157], v[40:41], v[122:123], v[156:157]
	v_pk_fma_f32 v[154:155], v[38:39], v[122:123], v[154:155]
	v_pk_fma_f32 v[152:153], v[36:37], v[122:123], v[152:153]
	v_pk_fma_f32 v[150:151], v[34:35], v[122:123], v[150:151]
	v_pk_fma_f32 v[148:149], v[32:33], v[122:123], v[148:149]
	v_pk_fma_f32 v[146:147], v[30:31], v[122:123], v[146:147]
	v_pk_fma_f32 v[144:145], v[28:29], v[122:123], v[144:145]
; #define LAS __attribute__((address_space(3)))
; __device__ __forceinline__ float bf_lo(unsigned w) { return __uint_as_float(w << 16); }
; __device__ __forceinline__ float bf_hi(unsigned w) { return __uint_as_float(w & 0xffff0000u); }
; __device__ __forceinline__ void phase_convpool(const Ctx& P, LAS unsigned char* lds, int vcu, int G) {
;     ...
;             for (int q = 0; q < 62; ++q) { const int j = t0 - 15 + q; unsigned w = 0u; if (j >= 0 && j < L) w = *(const unsigned*)(Z + (size_t)(rowbase + j) * 1024 + c0); zr[q] = (f32x2){bf_lo(w), bf_hi(w)}; }
; #pragma unroll
;             for (int tt = 0; tt < 32; ++tt) { f32x2 a = cb;
; #pragma unroll
;                 for (int k = 0; k < 31; ++k) a += wk[k] * zr[tt + k];
;                 *(LAS f32x2*)(tile + tt * 1024 + c0) = a; }
	v_pk_fma_f32 v[142:143], v[26:27], v[122:123], v[142:143]
	v_pk_fma_f32 v[140:141], v[24:25], v[122:123], v[140:141]
	v_pk_fma_f32 v[138:139], v[22:23], v[122:123], v[138:139]
	v_pk_fma_f32 v[122:123], v[20:21], v[122:123], v[124:125]
	v_lshlrev_b32_e32 v118, 16, v119
	v_and_b32_e32 v119, 0xffff0000, v119
	v_pk_fma_f32 v[182:183], v[68:69], v[120:121], v[182:183]
	v_pk_fma_f32 v[180:181], v[66:67], v[120:121], v[180:181]
	v_pk_fma_f32 v[178:179], v[64:65], v[120:121], v[178:179]
	v_pk_fma_f32 v[176:177], v[62:63], v[120:121], v[176:177]
	v_pk_fma_f32 v[174:175], v[60:61], v[120:121], v[174:175]
	v_pk_fma_f32 v[172:173], v[58:59], v[120:121], v[172:173]
	v_pk_fma_f32 v[170:171], v[56:57], v[120:121], v[170:171]
	v_pk_fma_f32 v[168:169], v[54:55], v[120:121], v[168:169]
	v_pk_fma_f32 v[166:167], v[52:53], v[120:121], v[166:167]
	v_pk_fma_f32 v[164:165], v[50:51], v[120:121], v[164:165]
	v_pk_fma_f32 v[162:163], v[48:49], v[120:121], v[162:163]
	v_pk_fma_f32 v[160:161], v[46:47], v[120:121], v[160:161]
	v_pk_fma_f32 v[158:159], v[44:45], v[120:121], v[158:159]
	v_pk_fma_f32 v[156:157], v[42:43], v[120:121], v[156:157]
	v_pk_fma_f32 v[154:155], v[40:41], v[120:121], v[154:155]
	v_pk_fma_f32 v[152:153], v[38:39], v[120:121], v[152:153]
	v_pk_fma_f32 v[150:151], v[36:37], v[120:121], v[150:151]
	v_pk_fma_f32 v[148:149], v[34:35], v[120:121], v[148:149]
	v_pk_fma_f32 v[146:147], v[32:33], v[120:121], v[146:147]
	v_pk_fma_f32 v[144:145], v[30:31], v[120:121], v[144:145]
	v_pk_fma_f32 v[142:143], v[28:29], v[120:121], v[142:143]
	v_pk_fma_f32 v[140:141], v[26:27], v[120:121], v[140:141]
	v_pk_fma_f32 v[138:139], v[24:25], v[120:121], v[138:139]
	v_pk_fma_f32 v[120:121], v[22:23], v[120:121], v[122:123]
	v_lshlrev_b32_e32 v116, 16, v117
	v_and_b32_e32 v117, 0xffff0000, v117
	v_pk_fma_f32 v[180:181], v[68:69], v[118:119], v[180:181]
	v_pk_fma_f32 v[178:179], v[66:67], v[118:119], v[178:179]
	v_pk_fma_f32 v[176:177], v[64:65], v[118:119], v[176:177]
	v_pk_fma_f32 v[174:175], v[62:63], v[118:119], v[174:175]
	v_pk_fma_f32 v[172:173], v[60:61], v[118:119], v[172:173]
	v_pk_fma_f32 v[170:171], v[58:59], v[118:119], v[170:171]
	v_pk_fma_f32 v[168:169], v[56:57], v[118:119], v[168:169]
	v_pk_fma_f32 v[166:167], v[54:55], v[118:119], v[166:167]
	v_pk_fma_f32 v[164:165], v[52:53], v[118:119], v[164:165]
	v_pk_fma_f32 v[162:163], v[50:51], v[118:119], v[162:163]
	v_pk_fma_f32 v[160:161], v[48:49], v[118:119], v[160:161]
	v_pk_fma_f32 v[158:159], v[46:47], v[118:119], v[158:159]
	v_pk_fma_f32 v[156:157], v[44:45], v[118:119], v[156:157]
	v_pk_fma_f32 v[154:155], v[42:43], v[118:119], v[154:155]
	v_pk_fma_f32 v[152:153], v[40:41], v[118:119], v[152:153]
	v_pk_fma_f32 v[150:151], v[38:39], v[118:119], v[150:151]
	v_pk_fma_f32 v[148:149], v[36:37], v[118:119], v[148:149]
	v_pk_fma_f32 v[146:147], v[34:35], v[118:119], v[146:147]
	v_pk_fma_f32 v[144:145], v[32:33], v[118:119], v[144:145]
	v_pk_fma_f32 v[142:143], v[30:31], v[118:119], v[142:143]
	v_pk_fma_f32 v[140:141], v[28:29], v[118:119], v[140:141]
	v_pk_fma_f32 v[138:139], v[26:27], v[118:119], v[138:139]
	v_pk_fma_f32 v[118:119], v[24:25], v[118:119], v[120:121]
	v_lshlrev_b32_e32 v114, 16, v115
	v_and_b32_e32 v115, 0xffff0000, v115
	v_pk_fma_f32 v[178:179], v[68:69], v[116:117], v[178:179]
	v_pk_fma_f32 v[176:177], v[66:67], v[116:117], v[176:177]
	v_pk_fma_f32 v[174:175], v[64:65], v[116:117], v[174:175]
	v_pk_fma_f32 v[172:173], v[62:63], v[116:117], v[172:173]
	v_pk_fma_f32 v[170:171], v[60:61], v[116:117], v[170:171]
	v_pk_fma_f32 v[168:169], v[58:59], v[116:117], v[168:169]
	v_pk_fma_f32 v[166:167], v[56:57], v[116:117], v[166:167]
	v_pk_fma_f32 v[164:165], v[54:55], v[116:117], v[164:165]
	v_pk_fma_f32 v[162:163], v[52:53], v[116:117], v[162:163]
	v_pk_fma_f32 v[160:161], v[50:51], v[116:117], v[160:161]
	v_pk_fma_f32 v[158:159], v[48:49], v[116:117], v[158:159]
	v_pk_fma_f32 v[156:157], v[46:47], v[116:117], v[156:157]
	v_pk_fma_f32 v[154:155], v[44:45], v[116:117], v[154:155]
	v_pk_fma_f32 v[152:153], v[42:43], v[116:117], v[152:153]
	v_pk_fma_f32 v[150:151], v[40:41], v[116:117], v[150:151]
	v_pk_fma_f32 v[148:149], v[38:39], v[116:117], v[148:149]
	v_pk_fma_f32 v[146:147], v[36:37], v[116:117], v[146:147]
	v_pk_fma_f32 v[144:145], v[34:35], v[116:117], v[144:145]
	v_pk_fma_f32 v[142:143], v[32:33], v[116:117], v[142:143]
	v_pk_fma_f32 v[140:141], v[30:31], v[116:117], v[140:141]
	v_pk_fma_f32 v[138:139], v[28:29], v[116:117], v[138:139]
	v_pk_fma_f32 v[116:117], v[26:27], v[116:117], v[118:119]
	v_lshlrev_b32_e32 v112, 16, v113
	v_and_b32_e32 v113, 0xffff0000, v113
	v_pk_fma_f32 v[176:177], v[68:69], v[114:115], v[176:177]
	v_pk_fma_f32 v[174:175], v[66:67], v[114:115], v[174:175]
	v_pk_fma_f32 v[172:173], v[64:65], v[114:115], v[172:173]
	v_pk_fma_f32 v[170:171], v[62:63], v[114:115], v[170:171]
	v_pk_fma_f32 v[168:169], v[60:61], v[114:115], v[168:169]
	v_pk_fma_f32 v[166:167], v[58:59], v[114:115], v[166:167]
	v_pk_fma_f32 v[164:165], v[56:57], v[114:115], v[164:165]
	v_pk_fma_f32 v[162:163], v[54:55], v[114:115], v[162:163]
	v_pk_fma_f32 v[160:161], v[52:53], v[114:115], v[160:161]
	v_pk_fma_f32 v[158:159], v[50:51], v[114:115], v[158:159]
	v_pk_fma_f32 v[156:157], v[48:49], v[114:115], v[156:157]
	v_pk_fma_f32 v[154:155], v[46:47], v[114:115], v[154:155]
	v_pk_fma_f32 v[152:153], v[44:45], v[114:115], v[152:153]
	v_pk_fma_f32 v[150:151], v[42:43], v[114:115], v[150:151]
	v_pk_fma_f32 v[148:149], v[40:41], v[114:115], v[148:149]
	v_pk_fma_f32 v[146:147], v[38:39], v[114:115], v[146:147]
	v_pk_fma_f32 v[144:145], v[36:37], v[114:115], v[144:145]
	v_pk_fma_f32 v[142:143], v[34:35], v[114:115], v[142:143]
; #define LAS __attribute__((address_space(3)))
; __device__ __forceinline__ float bf_lo(unsigned w) { return __uint_as_float(w << 16); }
; __device__ __forceinline__ float bf_hi(unsigned w) { return __uint_as_float(w & 0xffff0000u); }
; __device__ __forceinline__ void phase_convpool(const Ctx& P, LAS unsigned char* lds, int vcu, int G) {
;     ...
;             for (int q = 0; q < 62; ++q) { const int j = t0 - 15 + q; unsigned w = 0u; if (j >= 0 && j < L) w = *(const unsigned*)(Z + (size_t)(rowbase + j) * 1024 + c0); zr[q] = (f32x2){bf_lo(w), bf_hi(w)}; }
; #pragma unroll
;             for (int tt = 0; tt < 32; ++tt) { f32x2 a = cb;
; #pragma unroll
;                 for (int k = 0; k < 31; ++k) a += wk[k] * zr[tt + k];
;                 *(LAS f32x2*)(tile + tt * 1024 + c0) = a; }
	v_pk_fma_f32 v[140:141], v[32:33], v[114:115], v[140:141]
	v_pk_fma_f32 v[138:139], v[30:31], v[114:115], v[138:139]
	v_pk_fma_f32 v[114:115], v[28:29], v[114:115], v[116:117]
	v_lshlrev_b32_e32 v110, 16, v111
	v_and_b32_e32 v111, 0xffff0000, v111
	v_pk_fma_f32 v[174:175], v[68:69], v[112:113], v[174:175]
	v_pk_fma_f32 v[172:173], v[66:67], v[112:113], v[172:173]
	v_pk_fma_f32 v[170:171], v[64:65], v[112:113], v[170:171]
	v_pk_fma_f32 v[168:169], v[62:63], v[112:113], v[168:169]
	v_pk_fma_f32 v[166:167], v[60:61], v[112:113], v[166:167]
	v_pk_fma_f32 v[164:165], v[58:59], v[112:113], v[164:165]
	v_pk_fma_f32 v[162:163], v[56:57], v[112:113], v[162:163]
	v_pk_fma_f32 v[160:161], v[54:55], v[112:113], v[160:161]
	v_pk_fma_f32 v[158:159], v[52:53], v[112:113], v[158:159]
	v_pk_fma_f32 v[156:157], v[50:51], v[112:113], v[156:157]
	v_pk_fma_f32 v[154:155], v[48:49], v[112:113], v[154:155]
	v_pk_fma_f32 v[152:153], v[46:47], v[112:113], v[152:153]
	v_pk_fma_f32 v[150:151], v[44:45], v[112:113], v[150:151]
	v_pk_fma_f32 v[148:149], v[42:43], v[112:113], v[148:149]
	v_pk_fma_f32 v[146:147], v[40:41], v[112:113], v[146:147]
	v_pk_fma_f32 v[144:145], v[38:39], v[112:113], v[144:145]
	v_pk_fma_f32 v[142:143], v[36:37], v[112:113], v[142:143]
	v_pk_fma_f32 v[140:141], v[34:35], v[112:113], v[140:141]
	v_pk_fma_f32 v[138:139], v[32:33], v[112:113], v[138:139]
	v_pk_fma_f32 v[112:113], v[30:31], v[112:113], v[114:115]
	v_lshlrev_b32_e32 v108, 16, v109
	v_and_b32_e32 v109, 0xffff0000, v109
	v_pk_fma_f32 v[172:173], v[68:69], v[110:111], v[172:173]
	v_pk_fma_f32 v[170:171], v[66:67], v[110:111], v[170:171]
	v_pk_fma_f32 v[168:169], v[64:65], v[110:111], v[168:169]
	v_pk_fma_f32 v[166:167], v[62:63], v[110:111], v[166:167]
	v_pk_fma_f32 v[164:165], v[60:61], v[110:111], v[164:165]
	v_pk_fma_f32 v[162:163], v[58:59], v[110:111], v[162:163]
	v_pk_fma_f32 v[160:161], v[56:57], v[110:111], v[160:161]
	v_pk_fma_f32 v[158:159], v[54:55], v[110:111], v[158:159]
	v_pk_fma_f32 v[156:157], v[52:53], v[110:111], v[156:157]
	v_pk_fma_f32 v[154:155], v[50:51], v[110:111], v[154:155]
	v_pk_fma_f32 v[152:153], v[48:49], v[110:111], v[152:153]
	v_pk_fma_f32 v[150:151], v[46:47], v[110:111], v[150:151]
	v_pk_fma_f32 v[148:149], v[44:45], v[110:111], v[148:149]
	v_pk_fma_f32 v[146:147], v[42:43], v[110:111], v[146:147]
	v_pk_fma_f32 v[144:145], v[40:41], v[110:111], v[144:145]
	v_pk_fma_f32 v[142:143], v[38:39], v[110:111], v[142:143]
	v_pk_fma_f32 v[140:141], v[36:37], v[110:111], v[140:141]
	v_pk_fma_f32 v[138:139], v[34:35], v[110:111], v[138:139]
	v_pk_fma_f32 v[110:111], v[32:33], v[110:111], v[112:113]
	v_lshlrev_b32_e32 v106, 16, v107
	v_and_b32_e32 v107, 0xffff0000, v107
	v_pk_fma_f32 v[170:171], v[68:69], v[108:109], v[170:171]
	v_pk_fma_f32 v[168:169], v[66:67], v[108:109], v[168:169]
	v_pk_fma_f32 v[166:167], v[64:65], v[108:109], v[166:167]
	v_pk_fma_f32 v[164:165], v[62:63], v[108:109], v[164:165]
	v_pk_fma_f32 v[162:163], v[60:61], v[108:109], v[162:163]
	v_pk_fma_f32 v[160:161], v[58:59], v[108:109], v[160:161]
	v_pk_fma_f32 v[158:159], v[56:57], v[108:109], v[158:159]
	v_pk_fma_f32 v[156:157], v[54:55], v[108:109], v[156:157]
	v_pk_fma_f32 v[154:155], v[52:53], v[108:109], v[154:155]
	v_pk_fma_f32 v[152:153], v[50:51], v[108:109], v[152:153]
	v_pk_fma_f32 v[150:151], v[48:49], v[108:109], v[150:151]
	v_pk_fma_f32 v[148:149], v[46:47], v[108:109], v[148:149]
	v_pk_fma_f32 v[146:147], v[44:45], v[108:109], v[146:147]
	v_pk_fma_f32 v[144:145], v[42:43], v[108:109], v[144:145]
	v_pk_fma_f32 v[142:143], v[40:41], v[108:109], v[142:143]
	v_pk_fma_f32 v[140:141], v[38:39], v[108:109], v[140:141]
	v_pk_fma_f32 v[138:139], v[36:37], v[108:109], v[138:139]
	v_pk_fma_f32 v[108:109], v[34:35], v[108:109], v[110:111]
	v_lshlrev_b32_e32 v104, 16, v105
	v_and_b32_e32 v105, 0xffff0000, v105
	v_pk_fma_f32 v[168:169], v[68:69], v[106:107], v[168:169]
	v_pk_fma_f32 v[166:167], v[66:67], v[106:107], v[166:167]
	v_pk_fma_f32 v[164:165], v[64:65], v[106:107], v[164:165]
	v_pk_fma_f32 v[162:163], v[62:63], v[106:107], v[162:163]
	v_pk_fma_f32 v[160:161], v[60:61], v[106:107], v[160:161]
	v_pk_fma_f32 v[158:159], v[58:59], v[106:107], v[158:159]
	v_pk_fma_f32 v[156:157], v[56:57], v[106:107], v[156:157]
	v_pk_fma_f32 v[154:155], v[54:55], v[106:107], v[154:155]
	v_pk_fma_f32 v[152:153], v[52:53], v[106:107], v[152:153]
	v_pk_fma_f32 v[150:151], v[50:51], v[106:107], v[150:151]
	v_pk_fma_f32 v[148:149], v[48:49], v[106:107], v[148:149]
	v_pk_fma_f32 v[146:147], v[46:47], v[106:107], v[146:147]
	v_pk_fma_f32 v[144:145], v[44:45], v[106:107], v[144:145]
	v_pk_fma_f32 v[142:143], v[42:43], v[106:107], v[142:143]
	v_pk_fma_f32 v[140:141], v[40:41], v[106:107], v[140:141]
	v_pk_fma_f32 v[138:139], v[38:39], v[106:107], v[138:139]
	v_pk_fma_f32 v[106:107], v[36:37], v[106:107], v[108:109]
	v_lshlrev_b32_e32 v102, 16, v103
	v_and_b32_e32 v103, 0xffff0000, v103
	v_pk_fma_f32 v[166:167], v[68:69], v[104:105], v[166:167]
	v_pk_fma_f32 v[164:165], v[66:67], v[104:105], v[164:165]
	v_pk_fma_f32 v[162:163], v[64:65], v[104:105], v[162:163]
	v_pk_fma_f32 v[160:161], v[62:63], v[104:105], v[160:161]
	v_pk_fma_f32 v[158:159], v[60:61], v[104:105], v[158:159]
	v_pk_fma_f32 v[156:157], v[58:59], v[104:105], v[156:157]
	v_pk_fma_f32 v[154:155], v[56:57], v[104:105], v[154:155]
	v_pk_fma_f32 v[152:153], v[54:55], v[104:105], v[152:153]
	v_pk_fma_f32 v[150:151], v[52:53], v[104:105], v[150:151]
	v_pk_fma_f32 v[148:149], v[50:51], v[104:105], v[148:149]
	v_pk_fma_f32 v[146:147], v[48:49], v[104:105], v[146:147]
	v_pk_fma_f32 v[144:145], v[46:47], v[104:105], v[144:145]
; #define LAS __attribute__((address_space(3)))
; __device__ __forceinline__ float bf_lo(unsigned w) { return __uint_as_float(w << 16); }
; __device__ __forceinline__ float bf_hi(unsigned w) { return __uint_as_float(w & 0xffff0000u); }
; __device__ __forceinline__ void phase_convpool(const Ctx& P, LAS unsigned char* lds, int vcu, int G) {
;     ...
;             for (int q = 0; q < 62; ++q) { const int j = t0 - 15 + q; unsigned w = 0u; if (j >= 0 && j < L) w = *(const unsigned*)(Z + (size_t)(rowbase + j) * 1024 + c0); zr[q] = (f32x2){bf_lo(w), bf_hi(w)}; }
; #pragma unroll
;             for (int tt = 0; tt < 32; ++tt) { f32x2 a = cb;
; #pragma unroll
;                 for (int k = 0; k < 31; ++k) a += wk[k] * zr[tt + k];
;                 *(LAS f32x2*)(tile + tt * 1024 + c0) = a; }
	v_pk_fma_f32 v[142:143], v[44:45], v[104:105], v[142:143]
	v_pk_fma_f32 v[140:141], v[42:43], v[104:105], v[140:141]
	v_pk_fma_f32 v[138:139], v[40:41], v[104:105], v[138:139]
	v_pk_fma_f32 v[104:105], v[38:39], v[104:105], v[106:107]
	v_lshlrev_b32_e32 v100, 16, v101
	v_and_b32_e32 v101, 0xffff0000, v101
	v_pk_fma_f32 v[164:165], v[68:69], v[102:103], v[164:165]
	v_pk_fma_f32 v[162:163], v[66:67], v[102:103], v[162:163]
	v_pk_fma_f32 v[160:161], v[64:65], v[102:103], v[160:161]
	v_pk_fma_f32 v[158:159], v[62:63], v[102:103], v[158:159]
	v_pk_fma_f32 v[156:157], v[60:61], v[102:103], v[156:157]
	v_pk_fma_f32 v[154:155], v[58:59], v[102:103], v[154:155]
	v_pk_fma_f32 v[152:153], v[56:57], v[102:103], v[152:153]
	v_pk_fma_f32 v[150:151], v[54:55], v[102:103], v[150:151]
	v_pk_fma_f32 v[148:149], v[52:53], v[102:103], v[148:149]
	v_pk_fma_f32 v[146:147], v[50:51], v[102:103], v[146:147]
	v_pk_fma_f32 v[144:145], v[48:49], v[102:103], v[144:145]
	v_pk_fma_f32 v[142:143], v[46:47], v[102:103], v[142:143]
	v_pk_fma_f32 v[140:141], v[44:45], v[102:103], v[140:141]
	v_pk_fma_f32 v[138:139], v[42:43], v[102:103], v[138:139]
	v_pk_fma_f32 v[102:103], v[40:41], v[102:103], v[104:105]
	v_lshlrev_b32_e32 v98, 16, v99
	v_and_b32_e32 v99, 0xffff0000, v99
	v_pk_fma_f32 v[162:163], v[68:69], v[100:101], v[162:163]
	v_pk_fma_f32 v[160:161], v[66:67], v[100:101], v[160:161]
	v_pk_fma_f32 v[158:159], v[64:65], v[100:101], v[158:159]
	v_pk_fma_f32 v[156:157], v[62:63], v[100:101], v[156:157]
	v_pk_fma_f32 v[154:155], v[60:61], v[100:101], v[154:155]
	v_pk_fma_f32 v[152:153], v[58:59], v[100:101], v[152:153]
	v_pk_fma_f32 v[150:151], v[56:57], v[100:101], v[150:151]
	v_pk_fma_f32 v[148:149], v[54:55], v[100:101], v[148:149]
	v_pk_fma_f32 v[146:147], v[52:53], v[100:101], v[146:147]
	v_pk_fma_f32 v[144:145], v[50:51], v[100:101], v[144:145]
	v_pk_fma_f32 v[142:143], v[48:49], v[100:101], v[142:143]
	v_pk_fma_f32 v[140:141], v[46:47], v[100:101], v[140:141]
	v_pk_fma_f32 v[138:139], v[44:45], v[100:101], v[138:139]
	v_pk_fma_f32 v[100:101], v[42:43], v[100:101], v[102:103]
	v_lshlrev_b32_e32 v96, 16, v97
	v_and_b32_e32 v97, 0xffff0000, v97
	v_pk_fma_f32 v[160:161], v[68:69], v[98:99], v[160:161]
	v_pk_fma_f32 v[158:159], v[66:67], v[98:99], v[158:159]
	v_pk_fma_f32 v[156:157], v[64:65], v[98:99], v[156:157]
	v_pk_fma_f32 v[154:155], v[62:63], v[98:99], v[154:155]
	v_pk_fma_f32 v[152:153], v[60:61], v[98:99], v[152:153]
	v_pk_fma_f32 v[150:151], v[58:59], v[98:99], v[150:151]
	v_pk_fma_f32 v[148:149], v[56:57], v[98:99], v[148:149]
	v_pk_fma_f32 v[146:147], v[54:55], v[98:99], v[146:147]
	v_pk_fma_f32 v[144:145], v[52:53], v[98:99], v[144:145]
	v_pk_fma_f32 v[142:143], v[50:51], v[98:99], v[142:143]
	v_pk_fma_f32 v[140:141], v[48:49], v[98:99], v[140:141]
	v_pk_fma_f32 v[138:139], v[46:47], v[98:99], v[138:139]
	v_pk_fma_f32 v[98:99], v[44:45], v[98:99], v[100:101]
	v_lshlrev_b32_e32 v94, 16, v95
	v_and_b32_e32 v95, 0xffff0000, v95
	v_pk_fma_f32 v[158:159], v[68:69], v[96:97], v[158:159]
	v_pk_fma_f32 v[156:157], v[66:67], v[96:97], v[156:157]
	v_pk_fma_f32 v[154:155], v[64:65], v[96:97], v[154:155]
	v_pk_fma_f32 v[152:153], v[62:63], v[96:97], v[152:153]
	v_pk_fma_f32 v[150:151], v[60:61], v[96:97], v[150:151]
	v_pk_fma_f32 v[148:149], v[58:59], v[96:97], v[148:149]
	v_pk_fma_f32 v[146:147], v[56:57], v[96:97], v[146:147]
	v_pk_fma_f32 v[144:145], v[54:55], v[96:97], v[144:145]
	v_pk_fma_f32 v[142:143], v[52:53], v[96:97], v[142:143]
	v_pk_fma_f32 v[140:141], v[50:51], v[96:97], v[140:141]
	v_pk_fma_f32 v[138:139], v[48:49], v[96:97], v[138:139]
	v_pk_fma_f32 v[96:97], v[46:47], v[96:97], v[98:99]
	v_lshlrev_b32_e32 v92, 16, v93
	v_and_b32_e32 v93, 0xffff0000, v93
	v_pk_fma_f32 v[156:157], v[68:69], v[94:95], v[156:157]
	v_pk_fma_f32 v[154:155], v[66:67], v[94:95], v[154:155]
	v_pk_fma_f32 v[152:153], v[64:65], v[94:95], v[152:153]
	v_pk_fma_f32 v[150:151], v[62:63], v[94:95], v[150:151]
	v_pk_fma_f32 v[148:149], v[60:61], v[94:95], v[148:149]
	v_pk_fma_f32 v[146:147], v[58:59], v[94:95], v[146:147]
	v_pk_fma_f32 v[144:145], v[56:57], v[94:95], v[144:145]
	v_pk_fma_f32 v[142:143], v[54:55], v[94:95], v[142:143]
	v_pk_fma_f32 v[140:141], v[52:53], v[94:95], v[140:141]
	v_pk_fma_f32 v[138:139], v[50:51], v[94:95], v[138:139]
	v_pk_fma_f32 v[94:95], v[48:49], v[94:95], v[96:97]
	v_lshlrev_b32_e32 v90, 16, v91
	v_and_b32_e32 v91, 0xffff0000, v91
	v_pk_fma_f32 v[154:155], v[68:69], v[92:93], v[154:155]
	v_pk_fma_f32 v[152:153], v[66:67], v[92:93], v[152:153]
	v_pk_fma_f32 v[150:151], v[64:65], v[92:93], v[150:151]
	v_pk_fma_f32 v[148:149], v[62:63], v[92:93], v[148:149]
	v_pk_fma_f32 v[146:147], v[60:61], v[92:93], v[146:147]
	v_pk_fma_f32 v[144:145], v[58:59], v[92:93], v[144:145]
	v_pk_fma_f32 v[142:143], v[56:57], v[92:93], v[142:143]
	v_pk_fma_f32 v[140:141], v[54:55], v[92:93], v[140:141]
	v_pk_fma_f32 v[138:139], v[52:53], v[92:93], v[138:139]
	v_pk_fma_f32 v[92:93], v[50:51], v[92:93], v[94:95]
	v_lshlrev_b32_e32 v88, 16, v89
	v_and_b32_e32 v89, 0xffff0000, v89
	v_pk_fma_f32 v[152:153], v[68:69], v[90:91], v[152:153]
	v_pk_fma_f32 v[150:151], v[66:67], v[90:91], v[150:151]
	v_pk_fma_f32 v[148:149], v[64:65], v[90:91], v[148:149]
	v_pk_fma_f32 v[146:147], v[62:63], v[90:91], v[146:147]
	v_pk_fma_f32 v[144:145], v[60:61], v[90:91], v[144:145]
	v_pk_fma_f32 v[142:143], v[58:59], v[90:91], v[142:143]
	v_pk_fma_f32 v[140:141], v[56:57], v[90:91], v[140:141]
	v_pk_fma_f32 v[138:139], v[54:55], v[90:91], v[138:139]
	v_pk_fma_f32 v[90:91], v[52:53], v[90:91], v[92:93]
	v_lshlrev_b32_e32 v86, 16, v87
	v_and_b32_e32 v87, 0xffff0000, v87
; #define LAS __attribute__((address_space(3)))
; __device__ __forceinline__ float bf_lo(unsigned w) { return __uint_as_float(w << 16); }
; __device__ __forceinline__ float bf_hi(unsigned w) { return __uint_as_float(w & 0xffff0000u); }
; __device__ __forceinline__ float sum4(const f32x4 v) { return (v[0] + v[1]) + (v[2] + v[3]); }
; __device__ __forceinline__ void phase_convpool(const Ctx& P, LAS unsigned char* lds, int vcu, int G) {
;     ...
;             for (int q = 0; q < 62; ++q) { const int j = t0 - 15 + q; unsigned w = 0u; if (j >= 0 && j < L) w = *(const unsigned*)(Z + (size_t)(rowbase + j) * 1024 + c0); zr[q] = (f32x2){bf_lo(w), bf_hi(w)}; }
; #pragma unroll
;             for (int tt = 0; tt < 32; ++tt) { f32x2 a = cb;
; #pragma unroll
;                 for (int k = 0; k < 31; ++k) a += wk[k] * zr[tt + k];
;                 *(LAS f32x2*)(tile + tt * 1024 + c0) = a; }
;         }
;         __syncthreads();
; #pragma unroll
;         for (int q = 0; q < 4; ++q) { const int tt = wave * 4 + q; f32x4 v[4]; float s = 0.f;
; #pragma unroll
;             for (int j = 0; j < 4; ++j) { v[j] = *(const LAS f32x4*)(tile + tt * 1024 + 4 * lane + 256 * j); s += sum4(v[j]); }
;             const float mean = wave_sum(s) * (1.0f / 1024.0f); float s2 = 0.f;
	v_pk_fma_f32 v[150:151], v[68:69], v[88:89], v[150:151]
	v_pk_fma_f32 v[148:149], v[66:67], v[88:89], v[148:149]
	v_pk_fma_f32 v[146:147], v[64:65], v[88:89], v[146:147]
	v_pk_fma_f32 v[144:145], v[62:63], v[88:89], v[144:145]
	v_pk_fma_f32 v[142:143], v[60:61], v[88:89], v[142:143]
	v_pk_fma_f32 v[140:141], v[58:59], v[88:89], v[140:141]
	v_pk_fma_f32 v[138:139], v[56:57], v[88:89], v[138:139]
	v_pk_fma_f32 v[88:89], v[54:55], v[88:89], v[90:91]
	v_lshlrev_b32_e32 v84, 16, v85
	v_and_b32_e32 v85, 0xffff0000, v85
	v_pk_fma_f32 v[148:149], v[68:69], v[86:87], v[148:149]
	v_pk_fma_f32 v[146:147], v[66:67], v[86:87], v[146:147]
	v_pk_fma_f32 v[144:145], v[64:65], v[86:87], v[144:145]
	v_pk_fma_f32 v[142:143], v[62:63], v[86:87], v[142:143]
	v_pk_fma_f32 v[140:141], v[60:61], v[86:87], v[140:141]
	v_pk_fma_f32 v[138:139], v[58:59], v[86:87], v[138:139]
	v_pk_fma_f32 v[86:87], v[56:57], v[86:87], v[88:89]
	v_lshlrev_b32_e32 v82, 16, v83
	v_and_b32_e32 v83, 0xffff0000, v83
	v_pk_fma_f32 v[146:147], v[68:69], v[84:85], v[146:147]
	v_pk_fma_f32 v[144:145], v[66:67], v[84:85], v[144:145]
	v_pk_fma_f32 v[142:143], v[64:65], v[84:85], v[142:143]
	v_pk_fma_f32 v[140:141], v[62:63], v[84:85], v[140:141]
	v_pk_fma_f32 v[138:139], v[60:61], v[84:85], v[138:139]
	v_pk_fma_f32 v[84:85], v[58:59], v[84:85], v[86:87]
	v_lshlrev_b32_e32 v80, 16, v81
	v_and_b32_e32 v81, 0xffff0000, v81
	v_pk_fma_f32 v[144:145], v[68:69], v[82:83], v[144:145]
	v_pk_fma_f32 v[142:143], v[66:67], v[82:83], v[142:143]
	v_pk_fma_f32 v[140:141], v[64:65], v[82:83], v[140:141]
	v_pk_fma_f32 v[138:139], v[62:63], v[82:83], v[138:139]
	v_pk_fma_f32 v[82:83], v[60:61], v[82:83], v[84:85]
	v_lshlrev_b32_e32 v4, 16, v5
	v_and_b32_e32 v5, 0xffff0000, v5
	v_pk_fma_f32 v[142:143], v[68:69], v[80:81], v[142:143]
	v_pk_fma_f32 v[140:141], v[66:67], v[80:81], v[140:141]
	v_pk_fma_f32 v[138:139], v[64:65], v[80:81], v[138:139]
	v_pk_fma_f32 v[80:81], v[62:63], v[80:81], v[82:83]
	v_lshlrev_b32_e32 v2, 16, v3
	v_and_b32_e32 v3, 0xffff0000, v3
	v_pk_fma_f32 v[140:141], v[68:69], v[4:5], v[140:141]
	v_pk_fma_f32 v[138:139], v[66:67], v[4:5], v[138:139]
	v_pk_fma_f32 v[4:5], v[64:65], v[4:5], v[80:81]
	v_pk_fma_f32 v[138:139], v[68:69], v[2:3], v[138:139]
	v_pk_fma_f32 v[2:3], v[66:67], v[2:3], v[4:5]
	v_mov_b64_e32 v[80:81], s[4:5]
	v_pk_fma_f32 v[2:3], v[68:69], v[136:137], v[2:3]
	ds_write2st64_b64 v1, v[208:209], v[210:211] offset0:32 offset1:40
	ds_write2st64_b64 v1, v[186:187], v[184:185] offset0:48 offset1:56
	ds_write2st64_b64 v1, v[182:183], v[180:181] offset0:64 offset1:72
	ds_write2st64_b64 v1, v[178:179], v[176:177] offset0:80 offset1:88
	ds_write2st64_b64 v1, v[174:175], v[172:173] offset0:96 offset1:104
	ds_write2st64_b64 v1, v[170:171], v[168:169] offset0:112 offset1:120
	ds_write_b64 v189, v[166:167]
	ds_write_b64 v190, v[164:165]
	ds_write_b64 v191, v[162:163]
	ds_write_b64 v192, v[160:161]
	ds_write_b64 v193, v[158:159]
	ds_write_b64 v194, v[156:157]
	ds_write_b64 v195, v[154:155]
	ds_write_b64 v196, v[152:153]
	ds_write_b64 v197, v[150:151]
	ds_write_b64 v198, v[148:149]
	ds_write_b64 v199, v[146:147]
	ds_write_b64 v200, v[144:145]
	ds_write_b64 v201, v[142:143]
	ds_write_b64 v202, v[140:141]
	ds_write_b64 v203, v[138:139]
	ds_write_b64 v204, v[2:3]
	s_waitcnt lgkmcnt(0)
	s_barrier
	v_add_u32_e32 v83, s19, v188
	ds_read_b128 v[92:95], v83
	ds_read_b128 v[96:99], v83 offset:1024
	v_and_b32_e32 v2, 64, v206
	v_add_u32_e32 v108, 64, v2
	v_xor_b32_e32 v2, 1, v206
	v_cmp_lt_i32_e32 vcc, v2, v108
	s_waitcnt lgkmcnt(0)
	v_mov_b32_e32 v3, v94
	v_mov_b32_e32 v4, v92
	v_cndmask_b32_e32 v2, v206, v2, vcc
	v_lshlrev_b32_e32 v82, 2, v2
	v_mov_b32_e32 v2, v93
	v_mov_b32_e32 v5, v95
	v_pk_add_f32 v[2:3], v[2:3], v[4:5]
	ds_read_b128 v[100:103], v83 offset:2048
	v_add_f32_e32 v2, v2, v3
	v_add_f32_e32 v84, 0, v2
	ds_read_b128 v[2:5], v83 offset:3072
	v_mov_b32_e32 v86, v97
	v_mov_b32_e32 v87, v98
	v_mov_b32_e32 v104, v96
	v_mov_b32_e32 v105, v99
	v_pk_add_f32 v[86:87], v[86:87], v[104:105]
	s_waitcnt lgkmcnt(0)
	v_add_f32_e32 v104, v100, v101
	v_pk_add_f32 v[86:87], v[86:87], v[86:87] op_sel:[0,1] op_sel_hi:[1,0]
	v_add_f32_e32 v106, v102, v103
	v_mov_b32_e32 v85, v2
	v_mov_b32_e32 v87, v3
	v_mov_b32_e32 v105, v4
	v_mov_b32_e32 v107, v5
	v_pk_add_f32 v[84:85], v[84:85], v[86:87]
	v_pk_add_f32 v[86:87], v[104:105], v[106:107]
	v_xor_b32_e32 v83, 2, v206
	v_pk_add_f32 v[84:85], v[84:85], v[86:87]
	v_cmp_lt_i32_e32 vcc, v83, v108
	v_add_f32_e32 v84, v84, v85
	ds_bpermute_b32 v85, v82, v84
	v_cndmask_b32_e32 v83, v206, v83, vcc
	v_lshlrev_b32_e32 v83, 2, v83
	s_add_i32 s10, s31, s34
	s_add_i32 s12, s10, s18
	s_waitcnt lgkmcnt(0)
	v_add_f32_e32 v85, v84, v85
	ds_bpermute_b32 v86, v83, v85
	v_xor_b32_e32 v84, 4, v206
	v_cmp_lt_i32_e32 vcc, v84, v108
	s_ashr_i32 s13, s12, 31
	s_lshl_b64 s[12:13], s[12:13], 12
	v_cndmask_b32_e32 v84, v206, v84, vcc
	v_lshlrev_b32_e32 v84, 2, v84
	s_waitcnt lgkmcnt(0)
	v_add_f32_e32 v86, v85, v86
	ds_bpermute_b32 v87, v84, v86
	v_xor_b32_e32 v85, 8, v206
	v_cmp_lt_i32_e32 vcc, v85, v108
	s_add_i32 s30, s30, s39
	s_add_i32 s26, s26, s27
	v_cndmask_b32_e32 v85, v206, v85, vcc
	v_lshlrev_b32_e32 v85, 2, v85
	s_waitcnt lgkmcnt(0)
	v_add_f32_e32 v87, v86, v87
	ds_bpermute_b32 v104, v85, v87
	v_xor_b32_e32 v86, 16, v206
	v_cmp_lt_i32_e32 vcc, v86, v108
	s_waitcnt lgkmcnt(0)
	v_add_f32_e32 v104, v87, v104
	v_cndmask_b32_e32 v86, v206, v86, vcc
	v_lshlrev_b32_e32 v86, 2, v86
	ds_bpermute_b32 v105, v86, v104
	v_xor_b32_e32 v87, 32, v206
	v_cmp_lt_i32_e32 vcc, v87, v108
	s_waitcnt lgkmcnt(0)
	v_add_f32_e32 v104, v104, v105
	v_cndmask_b32_e32 v87, v206, v87, vcc
	v_lshlrev_b32_e32 v87, 2, v87
	ds_bpermute_b32 v105, v87, v104
	s_waitcnt lgkmcnt(0)
; #define LAS __attribute__((address_space(3)))
; __device__ __forceinline__ unsigned cvt_pk_bf16(float lo, float hi) { unsigned r; asm("v_cvt_pk_bf16_f32 %0, %1, %2" : "=v"(r) : "v"(lo), "v"(hi)); return r; }
; __device__ __forceinline__ float sum4(const f32x4 v) { return (v[0] + v[1]) + (v[2] + v[3]); }
; __device__ __forceinline__ float sq4(const f32x4 v) { return (v[0] * v[0] + v[1] * v[1]) + (v[2] * v[2] + v[3] * v[3]); }
; __device__ __forceinline__ float siluf_(float x) { return x * sigmoidf_(x); }
; __device__ __forceinline__ void phase_convpool(const Ctx& P, LAS unsigned char* lds, int vcu, int G) {
;     ...
;         for (int q = 0; q < 4; ++q) { const int tt = wave * 4 + q; f32x4 v[4]; float s = 0.f;
; #pragma unroll
;             for (int j = 0; j < 4; ++j) { v[j] = *(const LAS f32x4*)(tile + tt * 1024 + 4 * lane + 256 * j); s += sum4(v[j]); }
;             const float mean = wave_sum(s) * (1.0f / 1024.0f); float s2 = 0.f;
; #pragma unroll
;             for (int j = 0; j < 4; ++j) { v[j] = v[j] - mean; s2 += sq4(v[j]); }
;             const float rstd = __builtin_amdgcn_rsqf(wave_sum(s2) * (1.0f / 1024.0f) + EPS);
; #pragma unroll
;             for (int j = 0; j < 4; ++j) { const int c = 4 * lane + 256 * j; const f32x4 g4 = *(const f32x4*)(P.in[13] + c), b4 = *(const f32x4*)(P.in[14] + c); f32x4 y = v[j] * rstd * g4 + b4;
; #pragma unroll
;                 for (int e = 0; e < 4; ++e) y[e] = siluf_(y[e]);
;                 u32x2 w; w.x = cvt_pk_bf16(y[0], y[1]); w.y = cvt_pk_bf16(y[2], y[3]); *(u32x2*)(Y0 + (size_t)(rowbase + t0 + tt) * DM + 1024 + c) = w; } }
	v_add_f32_e32 v116, v104, v105
	v_mov_b64_e32 v[104:105], v[222:223]
	v_mov_b64_e32 v[106:107], v[224:225]
	v_mov_b64_e32 v[88:89], v[238:239]
	v_mov_b64_e32 v[90:91], v[240:241]
	v_fmamk_f32 v93, v116, 0xba800000, v93
	v_fmamk_f32 v92, v116, 0xba800000, v92
	v_fmamk_f32 v95, v116, 0xba800000, v95
	v_fmac_f32_e32 v94, 0xba800000, v116
	v_pk_mul_f32 v[108:109], v[94:95], v[94:95]
	v_pk_mul_f32 v[110:111], v[92:93], v[92:93]
	v_fmamk_f32 v97, v116, 0xba800000, v97
	v_pk_mov_b32 v[112:113], v[110:111], v[108:109] op_sel:[1,0]
	v_mov_b32_e32 v111, v109
	v_pk_add_f32 v[108:109], v[112:113], v[110:111]
	v_fmamk_f32 v96, v116, 0xba800000, v96
	v_fmamk_f32 v99, v116, 0xba800000, v99
	v_fmac_f32_e32 v98, 0xba800000, v116
	v_pk_add_f32 v[108:109], v[108:109], v[108:109] op_sel_hi:[0,1]
	v_pk_mul_f32 v[110:111], v[98:99], v[98:99]
	v_pk_mul_f32 v[112:113], v[96:97], v[96:97]
	v_fmamk_f32 v100, v116, 0xba800000, v100
	v_pk_mov_b32 v[114:115], v[112:113], v[110:111] op_sel:[1,0]
	v_mov_b32_e32 v113, v111
	v_fmamk_f32 v101, v116, 0xba800000, v101
	v_fmac_f32_e32 v102, 0xba800000, v116
	v_mul_f32_e32 v108, v100, v100
	v_pk_add_f32 v[110:111], v[114:115], v[112:113]
	v_fmamk_f32 v103, v116, 0xba800000, v103
	v_pk_fma_f32 v[112:113], v[100:101], v[100:101], v[108:109] op_sel_hi:[1,1,0]
	v_mul_f32_e32 v108, v102, v102
	v_pk_add_f32 v[110:111], v[110:111], v[110:111] op_sel_hi:[0,1]
	v_pk_fma_f32 v[114:115], v[102:103], v[102:103], v[108:109] op_sel_hi:[1,1,0]
	v_fmamk_f32 v5, v116, 0xba800000, v5
	v_fmamk_f32 v4, v116, 0xba800000, v4
	v_fmamk_f32 v3, v116, 0xba800000, v3
	v_fmac_f32_e32 v2, 0xba800000, v116
	v_mul_f32_e32 v112, v2, v2
	v_mul_f32_e32 v114, v3, v3
	v_mul_f32_e32 v108, v4, v4
	v_mul_f32_e32 v110, v5, v5
	v_pk_add_f32 v[112:113], v[112:113], v[114:115]
	v_pk_add_f32 v[108:109], v[108:109], v[110:111]
	s_nop 0
	v_pk_add_f32 v[108:109], v[112:113], v[108:109]
	s_nop 0
	v_add_f32_e32 v108, v108, v109
	ds_bpermute_b32 v109, v82, v108
	s_waitcnt lgkmcnt(0)
	v_add_f32_e32 v108, v108, v109
	ds_bpermute_b32 v109, v83, v108
	s_waitcnt lgkmcnt(0)
	v_add_f32_e32 v108, v108, v109
	ds_bpermute_b32 v109, v84, v108
	s_waitcnt lgkmcnt(0)
	v_add_f32_e32 v108, v108, v109
	ds_bpermute_b32 v109, v85, v108
	s_waitcnt lgkmcnt(0)
	v_add_f32_e32 v108, v108, v109
	ds_bpermute_b32 v109, v86, v108
	s_waitcnt lgkmcnt(0)
	v_add_f32_e32 v108, v108, v109
	ds_bpermute_b32 v109, v87, v108
	s_waitcnt lgkmcnt(0)
	v_add_f32_e32 v108, v108, v109
	v_fmamk_f32 v108, v108, 0x3a800000, v205
	v_rsq_f32_e32 v108, v108
	s_nop 0
	v_pk_mul_f32 v[92:93], v[92:93], v[108:109] op_sel_hi:[1,0]
	v_pk_mul_f32 v[94:95], v[94:95], v[108:109] op_sel_hi:[1,0]
	v_pk_fma_f32 v[88:89], v[104:105], v[92:93], v[88:89]
	v_pk_fma_f32 v[90:91], v[106:107], v[94:95], v[90:91]
	v_mul_f32_e32 v92, 0xbfb8aa3b, v88
	v_mul_f32_e32 v93, 0xbfb8aa3b, v89
	v_exp_f32_e32 v92, v92
	v_exp_f32_e32 v93, v93
	v_mul_f32_e32 v94, 0xbfb8aa3b, v90
	v_mul_f32_e32 v95, 0xbfb8aa3b, v91
	v_exp_f32_e32 v94, v94
	v_exp_f32_e32 v95, v95
	v_add_f32_e32 v92, 1.0, v92
	v_add_f32_e32 v93, 1.0, v93
	v_rcp_f32_e32 v92, v92
	v_rcp_f32_e32 v93, v93
	v_add_f32_e32 v94, 1.0, v94
	v_add_f32_e32 v95, 1.0, v95
	v_rcp_f32_e32 v94, v94
	v_rcp_f32_e32 v95, v95
	v_mul_f32_e32 v88, v88, v92
	v_mul_f32_e32 v89, v89, v93
	v_lshl_add_u64 v[104:105], v[78:79], 0, s[12:13]
	v_mul_f32_e32 v90, v90, v94
	v_mul_f32_e32 v91, v91, v95
	v_cvt_pk_bf16_f32 v88, v88, v89
	v_cvt_pk_bf16_f32 v89, v90, v91
	global_store_dwordx2 v[104:105], v[88:89], off offset:2048
	v_pk_mul_f32 v[96:97], v[96:97], v[108:109] op_sel_hi:[1,0]
	v_pk_mul_f32 v[98:99], v[98:99], v[108:109] op_sel_hi:[1,0]
	v_pk_mul_f32 v[2:3], v[2:3], v[108:109] op_sel_hi:[1,0]
	v_pk_mul_f32 v[4:5], v[4:5], v[108:109] op_sel_hi:[1,0]
	s_add_i32 s12, s10, s20
	s_ashr_i32 s13, s12, 31
	s_lshl_b64 s[12:13], s[12:13], 12
	s_waitcnt lgkmcnt(0)
	v_mov_b64_e32 v[92:93], v[226:227]
	v_mov_b64_e32 v[94:95], v[228:229]
	v_mov_b64_e32 v[88:89], v[242:243]
	v_mov_b64_e32 v[90:91], v[244:245]
	v_pk_fma_f32 v[88:89], v[92:93], v[96:97], v[88:89]
	s_nop 0
	v_mul_f32_e32 v92, 0xbfb8aa3b, v88
	v_mul_f32_e32 v93, 0xbfb8aa3b, v89
	v_pk_fma_f32 v[90:91], v[94:95], v[98:99], v[90:91]
	v_exp_f32_e32 v92, v92
	v_exp_f32_e32 v93, v93
	v_mul_f32_e32 v94, 0xbfb8aa3b, v90
	v_mul_f32_e32 v95, 0xbfb8aa3b, v91
	v_exp_f32_e32 v94, v94
	v_exp_f32_e32 v95, v95
	v_add_f32_e32 v92, 1.0, v92
	v_add_f32_e32 v93, 1.0, v93
	v_rcp_f32_e32 v92, v92
	v_rcp_f32_e32 v93, v93
	v_add_f32_e32 v94, 1.0, v94
	v_add_f32_e32 v95, 1.0, v95
	v_rcp_f32_e32 v94, v94
	v_rcp_f32_e32 v95, v95
	v_mul_f32_e32 v88, v88, v92
	v_mul_f32_e32 v89, v89, v93
	v_mul_f32_e32 v90, v90, v94
	v_mul_f32_e32 v91, v91, v95
	v_cvt_pk_bf16_f32 v88, v88, v89
	v_cvt_pk_bf16_f32 v89, v90, v91
	global_store_dwordx2 v[104:105], v[88:89], off offset:2560
	v_pk_mul_f32 v[96:97], v[100:101], v[108:109] op_sel_hi:[1,0]
	v_pk_mul_f32 v[98:99], v[102:103], v[108:109] op_sel_hi:[1,0]
	v_add_u32_e32 v100, s21, v188
	s_waitcnt lgkmcnt(0)
	v_mov_b64_e32 v[92:93], v[230:231]
	v_mov_b64_e32 v[94:95], v[232:233]
	v_mov_b64_e32 v[88:89], v[246:247]
	v_mov_b64_e32 v[90:91], v[248:249]
	v_pk_fma_f32 v[88:89], v[92:93], v[96:97], v[88:89]
	s_nop 0
	v_mul_f32_e32 v92, 0xbfb8aa3b, v88
	v_mul_f32_e32 v93, 0xbfb8aa3b, v89
	v_pk_fma_f32 v[90:91], v[94:95], v[98:99], v[90:91]
	v_exp_f32_e32 v92, v92
	v_exp_f32_e32 v93, v93
	v_mul_f32_e32 v94, 0xbfb8aa3b, v90
	v_mul_f32_e32 v95, 0xbfb8aa3b, v91
	v_exp_f32_e32 v94, v94
	v_exp_f32_e32 v95, v95
	v_add_f32_e32 v92, 1.0, v92
	v_add_f32_e32 v93, 1.0, v93
	v_rcp_f32_e32 v92, v92
	v_rcp_f32_e32 v93, v93
	v_add_f32_e32 v94, 1.0, v94
	v_add_f32_e32 v95, 1.0, v95
	v_rcp_f32_e32 v94, v94
	v_rcp_f32_e32 v95, v95
	v_mul_f32_e32 v88, v88, v92
	v_mul_f32_e32 v89, v89, v93
	v_mul_f32_e32 v90, v90, v94
	v_mul_f32_e32 v91, v91, v95
	v_cvt_pk_bf16_f32 v88, v88, v89
	v_cvt_pk_bf16_f32 v89, v90, v91
	global_store_dwordx2 v[104:105], v[88:89], off offset:3072
	s_waitcnt lgkmcnt(0)
; #define LAS __attribute__((address_space(3)))
; __device__ __forceinline__ unsigned cvt_pk_bf16(float lo, float hi) { unsigned r; asm("v_cvt_pk_bf16_f32 %0, %1, %2" : "=v"(r) : "v"(lo), "v"(hi)); return r; }
; __device__ __forceinline__ float sum4(const f32x4 v) { return (v[0] + v[1]) + (v[2] + v[3]); }
; __device__ __forceinline__ float sq4(const f32x4 v) { return (v[0] * v[0] + v[1] * v[1]) + (v[2] * v[2] + v[3] * v[3]); }
; __device__ __forceinline__ float siluf_(float x) { return x * sigmoidf_(x); }
; __device__ __forceinline__ void phase_convpool(const Ctx& P, LAS unsigned char* lds, int vcu, int G) {
;     ...
;         for (int q = 0; q < 4; ++q) { const int tt = wave * 4 + q; f32x4 v[4]; float s = 0.f;
; #pragma unroll
;             for (int j = 0; j < 4; ++j) { v[j] = *(const LAS f32x4*)(tile + tt * 1024 + 4 * lane + 256 * j); s += sum4(v[j]); }
;             const float mean = wave_sum(s) * (1.0f / 1024.0f); float s2 = 0.f;
; #pragma unroll
;             for (int j = 0; j < 4; ++j) { v[j] = v[j] - mean; s2 += sq4(v[j]); }
;             const float rstd = __builtin_amdgcn_rsqf(wave_sum(s2) * (1.0f / 1024.0f) + EPS);
; #pragma unroll
;             for (int j = 0; j < 4; ++j) { const int c = 4 * lane + 256 * j; const f32x4 g4 = *(const f32x4*)(P.in[13] + c), b4 = *(const f32x4*)(P.in[14] + c); f32x4 y = v[j] * rstd * g4 + b4;
; #pragma unroll
;                 for (int e = 0; e < 4; ++e) y[e] = siluf_(y[e]);
;                 u32x2 w; w.x = cvt_pk_bf16(y[0], y[1]); w.y = cvt_pk_bf16(y[2], y[3]); *(u32x2*)(Y0 + (size_t)(rowbase + t0 + tt) * DM + 1024 + c) = w; } }
	v_mov_b64_e32 v[92:93], v[234:235]
	v_mov_b64_e32 v[94:95], v[236:237]
	v_mov_b64_e32 v[88:89], v[250:251]
	v_mov_b64_e32 v[90:91], v[252:253]
	v_pk_fma_f32 v[2:3], v[2:3], v[92:93], v[88:89]
	s_nop 0
	v_mul_f32_e32 v88, 0xbfb8aa3b, v2
	v_mul_f32_e32 v89, 0xbfb8aa3b, v3
	v_pk_fma_f32 v[4:5], v[4:5], v[94:95], v[90:91]
	v_exp_f32_e32 v88, v88
	v_exp_f32_e32 v89, v89
	v_mul_f32_e32 v90, 0xbfb8aa3b, v4
	v_mul_f32_e32 v91, 0xbfb8aa3b, v5
	v_exp_f32_e32 v90, v90
	v_exp_f32_e32 v91, v91
	v_add_f32_e32 v88, 1.0, v88
	v_add_f32_e32 v89, 1.0, v89
	v_rcp_f32_e32 v88, v88
	v_rcp_f32_e32 v89, v89
	v_add_f32_e32 v90, 1.0, v90
	v_add_f32_e32 v91, 1.0, v91
	v_rcp_f32_e32 v90, v90
	v_rcp_f32_e32 v91, v91
	v_mul_f32_e32 v2, v2, v88
	v_mul_f32_e32 v3, v3, v89
	v_mul_f32_e32 v4, v4, v90
	v_mul_f32_e32 v5, v5, v91
	v_cvt_pk_bf16_f32 v2, v2, v3
	v_cvt_pk_bf16_f32 v3, v4, v5
	global_store_dwordx2 v[104:105], v[2:3], off offset:3584
	ds_read_b128 v[88:91], v100
	ds_read_b128 v[92:95], v100 offset:1024
	s_waitcnt lgkmcnt(0)
	v_mov_b32_e32 v96, v89
	v_mov_b32_e32 v97, v90
	v_mov_b32_e32 v98, v88
	v_mov_b32_e32 v99, v91
	v_pk_add_f32 v[96:97], v[96:97], v[98:99]
	v_mov_b32_e32 v106, v93
	v_add_f32_e32 v96, v96, v97
	v_add_f32_e32 v104, 0, v96
	ds_read_b128 v[96:99], v100 offset:2048
	ds_read_b128 v[100:103], v100 offset:3072
	v_mov_b32_e32 v107, v94
	v_mov_b32_e32 v108, v92
	v_mov_b32_e32 v109, v95
	v_pk_add_f32 v[106:107], v[106:107], v[108:109]
	s_waitcnt lgkmcnt(0)
	v_add_f32_e32 v108, v96, v97
	v_pk_add_f32 v[106:107], v[106:107], v[106:107] op_sel:[0,1] op_sel_hi:[1,0]
	v_add_f32_e32 v110, v98, v99
	v_mov_b32_e32 v105, v100
	v_mov_b32_e32 v107, v101
	v_mov_b32_e32 v109, v102
	v_mov_b32_e32 v111, v103
	v_pk_add_f32 v[104:105], v[104:105], v[106:107]
	v_pk_add_f32 v[106:107], v[108:109], v[110:111]
	v_pk_add_f32 v[104:105], v[104:105], v[106:107]
	s_nop 0
	v_add_f32_e32 v104, v104, v105
	ds_bpermute_b32 v105, v82, v104
	s_waitcnt lgkmcnt(0)
	v_add_f32_e32 v104, v104, v105
	ds_bpermute_b32 v105, v83, v104
	s_waitcnt lgkmcnt(0)
	v_add_f32_e32 v104, v104, v105
	ds_bpermute_b32 v105, v84, v104
	s_waitcnt lgkmcnt(0)
	v_add_f32_e32 v104, v104, v105
	ds_bpermute_b32 v105, v85, v104
	s_waitcnt lgkmcnt(0)
	v_add_f32_e32 v104, v104, v105
	ds_bpermute_b32 v105, v86, v104
	s_waitcnt lgkmcnt(0)
	v_add_f32_e32 v104, v104, v105
	ds_bpermute_b32 v105, v87, v104
	s_waitcnt lgkmcnt(0)
	v_add_f32_e32 v116, v104, v105
	v_mov_b64_e32 v[104:105], v[222:223]
	v_mov_b64_e32 v[106:107], v[224:225]
	v_mov_b64_e32 v[2:3], v[238:239]
	v_mov_b64_e32 v[4:5], v[240:241]
	v_fmamk_f32 v89, v116, 0xba800000, v89
	v_fmamk_f32 v88, v116, 0xba800000, v88
	v_fmamk_f32 v91, v116, 0xba800000, v91
	v_fmac_f32_e32 v90, 0xba800000, v116
	v_pk_mul_f32 v[108:109], v[90:91], v[90:91]
	v_pk_mul_f32 v[110:111], v[88:89], v[88:89]
	v_fmamk_f32 v93, v116, 0xba800000, v93
	v_pk_mov_b32 v[112:113], v[110:111], v[108:109] op_sel:[1,0]
	v_mov_b32_e32 v111, v109
	v_pk_add_f32 v[108:109], v[112:113], v[110:111]
	v_fmamk_f32 v92, v116, 0xba800000, v92
	v_fmamk_f32 v95, v116, 0xba800000, v95
	v_fmac_f32_e32 v94, 0xba800000, v116
	v_pk_add_f32 v[108:109], v[108:109], v[108:109] op_sel_hi:[0,1]
	v_pk_mul_f32 v[110:111], v[94:95], v[94:95]
	v_pk_mul_f32 v[112:113], v[92:93], v[92:93]
	v_fmamk_f32 v96, v116, 0xba800000, v96
	v_pk_mov_b32 v[114:115], v[112:113], v[110:111] op_sel:[1,0]
	v_mov_b32_e32 v113, v111
	v_fmamk_f32 v97, v116, 0xba800000, v97
	v_fmac_f32_e32 v98, 0xba800000, v116
	v_mul_f32_e32 v108, v96, v96
	v_pk_add_f32 v[110:111], v[114:115], v[112:113]
	v_fmamk_f32 v99, v116, 0xba800000, v99
	v_pk_fma_f32 v[112:113], v[96:97], v[96:97], v[108:109] op_sel_hi:[1,1,0]
	v_mul_f32_e32 v108, v98, v98
	v_pk_add_f32 v[110:111], v[110:111], v[110:111] op_sel_hi:[0,1]
	v_pk_fma_f32 v[114:115], v[98:99], v[98:99], v[108:109] op_sel_hi:[1,1,0]
	v_fmamk_f32 v103, v116, 0xba800000, v103
	v_fmamk_f32 v102, v116, 0xba800000, v102
	v_fmamk_f32 v101, v116, 0xba800000, v101
	v_fmac_f32_e32 v100, 0xba800000, v116
	v_mul_f32_e32 v112, v100, v100
	v_mul_f32_e32 v114, v101, v101
	v_mul_f32_e32 v108, v102, v102
	v_mul_f32_e32 v110, v103, v103
	v_pk_add_f32 v[112:113], v[112:113], v[114:115]
	v_pk_add_f32 v[108:109], v[108:109], v[110:111]
	s_nop 0
	v_pk_add_f32 v[108:109], v[112:113], v[108:109]
	s_nop 0
	v_add_f32_e32 v108, v108, v109
	ds_bpermute_b32 v109, v82, v108
	s_waitcnt lgkmcnt(0)
	v_add_f32_e32 v108, v108, v109
	ds_bpermute_b32 v109, v83, v108
	s_waitcnt lgkmcnt(0)
	v_add_f32_e32 v108, v108, v109
	ds_bpermute_b32 v109, v84, v108
	s_waitcnt lgkmcnt(0)
	v_add_f32_e32 v108, v108, v109
	ds_bpermute_b32 v109, v85, v108
	s_waitcnt lgkmcnt(0)
	v_add_f32_e32 v108, v108, v109
	ds_bpermute_b32 v109, v86, v108
	s_waitcnt lgkmcnt(0)
	v_add_f32_e32 v108, v108, v109
	ds_bpermute_b32 v109, v87, v108
	s_waitcnt lgkmcnt(0)
	v_add_f32_e32 v108, v108, v109
	v_fmamk_f32 v108, v108, 0x3a800000, v205
	v_rsq_f32_e32 v108, v108
	s_nop 0
	v_pk_mul_f32 v[88:89], v[88:89], v[108:109] op_sel_hi:[1,0]
	v_pk_mul_f32 v[90:91], v[90:91], v[108:109] op_sel_hi:[1,0]
	v_pk_fma_f32 v[2:3], v[104:105], v[88:89], v[2:3]
	v_pk_fma_f32 v[4:5], v[106:107], v[90:91], v[4:5]
	v_mul_f32_e32 v88, 0xbfb8aa3b, v2
	v_mul_f32_e32 v89, 0xbfb8aa3b, v3
	v_exp_f32_e32 v88, v88
	v_exp_f32_e32 v89, v89
	v_mul_f32_e32 v90, 0xbfb8aa3b, v4
	v_mul_f32_e32 v91, 0xbfb8aa3b, v5
	v_exp_f32_e32 v90, v90
	v_exp_f32_e32 v91, v91
	v_add_f32_e32 v88, 1.0, v88
	v_add_f32_e32 v89, 1.0, v89
	v_rcp_f32_e32 v88, v88
	v_rcp_f32_e32 v89, v89
	v_add_f32_e32 v90, 1.0, v90
	v_add_f32_e32 v91, 1.0, v91
	v_rcp_f32_e32 v90, v90
	v_rcp_f32_e32 v91, v91
	v_mul_f32_e32 v2, v2, v88
	v_mul_f32_e32 v3, v3, v89
	v_lshl_add_u64 v[104:105], v[78:79], 0, s[12:13]
	v_mul_f32_e32 v4, v4, v90
	v_mul_f32_e32 v5, v5, v91
	v_cvt_pk_bf16_f32 v2, v2, v3
	v_cvt_pk_bf16_f32 v3, v4, v5
	global_store_dwordx2 v[104:105], v[2:3], off offset:2048
	v_pk_mul_f32 v[92:93], v[92:93], v[108:109] op_sel_hi:[1,0]
	v_pk_mul_f32 v[94:95], v[94:95], v[108:109] op_sel_hi:[1,0]
	s_add_i32 s12, s10, s22
	s_ashr_i32 s13, s12, 31
	s_lshl_b64 s[12:13], s[12:13], 12
	s_add_i32 s10, s10, s24
	s_ashr_i32 s11, s10, 31
	s_lshl_b64 s[10:11], s[10:11], 12
	s_cmpk_lt_i32 s30, 0x220
	s_waitcnt lgkmcnt(0)
; #define LAS __attribute__((address_space(3)))
; __device__ __forceinline__ unsigned cvt_pk_bf16(float lo, float hi) { unsigned r; asm("v_cvt_pk_bf16_f32 %0, %1, %2" : "=v"(r) : "v"(lo), "v"(hi)); return r; }
; __device__ __forceinline__ float sum4(const f32x4 v) { return (v[0] + v[1]) + (v[2] + v[3]); }
; __device__ __forceinline__ float sq4(const f32x4 v) { return (v[0] * v[0] + v[1] * v[1]) + (v[2] * v[2] + v[3] * v[3]); }
; __device__ __forceinline__ float siluf_(float x) { return x * sigmoidf_(x); }
; __device__ __forceinline__ void phase_convpool(const Ctx& P, LAS unsigned char* lds, int vcu, int G) {
;     ...
;         for (int q = 0; q < 4; ++q) { const int tt = wave * 4 + q; f32x4 v[4]; float s = 0.f;
; #pragma unroll
;             for (int j = 0; j < 4; ++j) { v[j] = *(const LAS f32x4*)(tile + tt * 1024 + 4 * lane + 256 * j); s += sum4(v[j]); }
;             const float mean = wave_sum(s) * (1.0f / 1024.0f); float s2 = 0.f;
; #pragma unroll
;             for (int j = 0; j < 4; ++j) { v[j] = v[j] - mean; s2 += sq4(v[j]); }
;             const float rstd = __builtin_amdgcn_rsqf(wave_sum(s2) * (1.0f / 1024.0f) + EPS);
; #pragma unroll
;             for (int j = 0; j < 4; ++j) { const int c = 4 * lane + 256 * j; const f32x4 g4 = *(const f32x4*)(P.in[13] + c), b4 = *(const f32x4*)(P.in[14] + c); f32x4 y = v[j] * rstd * g4 + b4;
; #pragma unroll
;                 for (int e = 0; e < 4; ++e) y[e] = siluf_(y[e]);
;                 u32x2 w; w.x = cvt_pk_bf16(y[0], y[1]); w.y = cvt_pk_bf16(y[2], y[3]); *(u32x2*)(Y0 + (size_t)(rowbase + t0 + tt) * DM + 1024 + c) = w; } }
	v_mov_b64_e32 v[88:89], v[226:227]
	v_mov_b64_e32 v[90:91], v[228:229]
	v_mov_b64_e32 v[2:3], v[242:243]
	v_mov_b64_e32 v[4:5], v[244:245]
	v_pk_fma_f32 v[2:3], v[88:89], v[92:93], v[2:3]
	s_nop 0
	v_mul_f32_e32 v88, 0xbfb8aa3b, v2
	v_mul_f32_e32 v89, 0xbfb8aa3b, v3
	v_pk_fma_f32 v[4:5], v[90:91], v[94:95], v[4:5]
	v_exp_f32_e32 v88, v88
	v_exp_f32_e32 v89, v89
	v_mul_f32_e32 v90, 0xbfb8aa3b, v4
	v_mul_f32_e32 v91, 0xbfb8aa3b, v5
	v_exp_f32_e32 v90, v90
	v_exp_f32_e32 v91, v91
	v_add_f32_e32 v88, 1.0, v88
	v_add_f32_e32 v89, 1.0, v89
	v_rcp_f32_e32 v88, v88
	v_rcp_f32_e32 v89, v89
	v_add_f32_e32 v90, 1.0, v90
	v_add_f32_e32 v91, 1.0, v91
	v_rcp_f32_e32 v90, v90
	v_rcp_f32_e32 v91, v91
	v_mul_f32_e32 v2, v2, v88
	v_mul_f32_e32 v3, v3, v89
	v_mul_f32_e32 v4, v4, v90
	v_mul_f32_e32 v5, v5, v91
	v_cvt_pk_bf16_f32 v2, v2, v3
	v_cvt_pk_bf16_f32 v3, v4, v5
	global_store_dwordx2 v[104:105], v[2:3], off offset:2560
	v_pk_mul_f32 v[92:93], v[96:97], v[108:109] op_sel_hi:[1,0]
	v_pk_mul_f32 v[94:95], v[98:99], v[108:109] op_sel_hi:[1,0]
	s_waitcnt lgkmcnt(0)
	v_mov_b64_e32 v[88:89], v[230:231]
	v_mov_b64_e32 v[90:91], v[232:233]
	v_mov_b64_e32 v[2:3], v[246:247]
	v_mov_b64_e32 v[4:5], v[248:249]
	v_pk_fma_f32 v[2:3], v[88:89], v[92:93], v[2:3]
	s_nop 0
	v_mul_f32_e32 v88, 0xbfb8aa3b, v2
	v_mul_f32_e32 v89, 0xbfb8aa3b, v3
	v_pk_fma_f32 v[4:5], v[90:91], v[94:95], v[4:5]
	v_exp_f32_e32 v88, v88
	v_exp_f32_e32 v89, v89
	v_mul_f32_e32 v90, 0xbfb8aa3b, v4
	v_mul_f32_e32 v91, 0xbfb8aa3b, v5
	v_exp_f32_e32 v90, v90
	v_exp_f32_e32 v91, v91
	v_add_f32_e32 v88, 1.0, v88
	v_add_f32_e32 v89, 1.0, v89
	v_rcp_f32_e32 v88, v88
	v_rcp_f32_e32 v89, v89
	v_add_f32_e32 v90, 1.0, v90
	v_add_f32_e32 v91, 1.0, v91
	v_rcp_f32_e32 v90, v90
	v_rcp_f32_e32 v91, v91
	v_mul_f32_e32 v2, v2, v88
	v_mul_f32_e32 v3, v3, v89
	v_mul_f32_e32 v4, v4, v90
	v_mul_f32_e32 v5, v5, v91
	v_cvt_pk_bf16_f32 v2, v2, v3
	v_cvt_pk_bf16_f32 v3, v4, v5
	global_store_dwordx2 v[104:105], v[2:3], off offset:3072
	v_pk_mul_f32 v[92:93], v[100:101], v[108:109] op_sel_hi:[1,0]
	v_pk_mul_f32 v[94:95], v[102:103], v[108:109] op_sel_hi:[1,0]
	s_waitcnt lgkmcnt(0)
	v_mov_b64_e32 v[88:89], v[234:235]
	v_mov_b64_e32 v[90:91], v[236:237]
	v_mov_b64_e32 v[2:3], v[250:251]
	v_mov_b64_e32 v[4:5], v[252:253]
	v_pk_fma_f32 v[2:3], v[92:93], v[88:89], v[2:3]
	s_nop 0
	v_mul_f32_e32 v88, 0xbfb8aa3b, v2
	v_mul_f32_e32 v89, 0xbfb8aa3b, v3
	v_pk_fma_f32 v[4:5], v[94:95], v[90:91], v[4:5]
	v_exp_f32_e32 v88, v88
	v_exp_f32_e32 v89, v89
	v_mul_f32_e32 v90, 0xbfb8aa3b, v4
	v_mul_f32_e32 v91, 0xbfb8aa3b, v5
	v_exp_f32_e32 v90, v90
	v_exp_f32_e32 v91, v91
	v_add_f32_e32 v88, 1.0, v88
	v_add_f32_e32 v89, 1.0, v89
	v_rcp_f32_e32 v88, v88
	v_rcp_f32_e32 v89, v89
	v_add_f32_e32 v90, 1.0, v90
	v_add_f32_e32 v91, 1.0, v91
	v_rcp_f32_e32 v90, v90
	v_rcp_f32_e32 v91, v91
	v_mul_f32_e32 v2, v2, v88
	v_mul_f32_e32 v3, v3, v89
	v_mul_f32_e32 v4, v4, v90
	v_mul_f32_e32 v5, v5, v91
	v_cvt_pk_bf16_f32 v2, v2, v3
	v_cvt_pk_bf16_f32 v3, v4, v5
	global_store_dwordx2 v[104:105], v[2:3], off offset:3584
	v_add_u32_e32 v105, s23, v188
	ds_read_b128 v[92:95], v105
	ds_read_b128 v[96:99], v105 offset:1024
	ds_read_b128 v[100:103], v105 offset:2048
	s_waitcnt lgkmcnt(0)
	v_mov_b32_e32 v2, v93
	v_mov_b32_e32 v3, v94
	v_mov_b32_e32 v4, v92
	v_mov_b32_e32 v5, v95
	v_pk_add_f32 v[2:3], v[2:3], v[4:5]
	v_mov_b32_e32 v106, v97
	v_add_f32_e32 v2, v2, v3
	v_add_f32_e32 v104, 0, v2
	ds_read_b128 v[2:5], v105 offset:3072
	v_mov_b32_e32 v107, v98
	v_mov_b32_e32 v108, v96
	v_mov_b32_e32 v109, v99
	v_pk_add_f32 v[106:107], v[106:107], v[108:109]
	v_add_f32_e32 v108, v100, v101
	v_pk_add_f32 v[106:107], v[106:107], v[106:107] op_sel:[0,1] op_sel_hi:[1,0]
	v_add_f32_e32 v110, v102, v103
	s_waitcnt lgkmcnt(0)
	v_mov_b32_e32 v105, v2
	v_mov_b32_e32 v107, v3
	v_mov_b32_e32 v109, v4
	v_mov_b32_e32 v111, v5
	v_pk_add_f32 v[104:105], v[104:105], v[106:107]
	v_pk_add_f32 v[106:107], v[108:109], v[110:111]
	v_pk_add_f32 v[104:105], v[104:105], v[106:107]
	s_nop 0
	v_add_f32_e32 v104, v104, v105
	ds_bpermute_b32 v105, v82, v104
	s_waitcnt lgkmcnt(0)
	v_add_f32_e32 v104, v104, v105
	ds_bpermute_b32 v105, v83, v104
	s_waitcnt lgkmcnt(0)
	v_add_f32_e32 v104, v104, v105
	ds_bpermute_b32 v105, v84, v104
	s_waitcnt lgkmcnt(0)
	v_add_f32_e32 v104, v104, v105
	ds_bpermute_b32 v105, v85, v104
	s_waitcnt lgkmcnt(0)
	v_add_f32_e32 v104, v104, v105
	ds_bpermute_b32 v105, v86, v104
	s_waitcnt lgkmcnt(0)
	v_add_f32_e32 v104, v104, v105
	ds_bpermute_b32 v105, v87, v104
	s_waitcnt lgkmcnt(0)
	v_add_f32_e32 v116, v104, v105
	v_mov_b64_e32 v[104:105], v[222:223]
	v_mov_b64_e32 v[106:107], v[224:225]
	v_mov_b64_e32 v[88:89], v[238:239]
	v_mov_b64_e32 v[90:91], v[240:241]
	v_fmamk_f32 v93, v116, 0xba800000, v93
	v_fmamk_f32 v92, v116, 0xba800000, v92
	v_fmamk_f32 v95, v116, 0xba800000, v95
	v_fmac_f32_e32 v94, 0xba800000, v116
	v_pk_mul_f32 v[108:109], v[94:95], v[94:95]
	v_pk_mul_f32 v[110:111], v[92:93], v[92:93]
	v_fmamk_f32 v97, v116, 0xba800000, v97
	v_pk_mov_b32 v[112:113], v[110:111], v[108:109] op_sel:[1,0]
	v_mov_b32_e32 v111, v109
	v_pk_add_f32 v[108:109], v[112:113], v[110:111]
	v_fmamk_f32 v96, v116, 0xba800000, v96
	v_fmamk_f32 v99, v116, 0xba800000, v99
	v_fmac_f32_e32 v98, 0xba800000, v116
	v_pk_add_f32 v[108:109], v[108:109], v[108:109] op_sel_hi:[0,1]
	v_pk_mul_f32 v[110:111], v[98:99], v[98:99]
	v_pk_mul_f32 v[112:113], v[96:97], v[96:97]
	v_fmamk_f32 v100, v116, 0xba800000, v100
	v_pk_mov_b32 v[114:115], v[112:113], v[110:111] op_sel:[1,0]
	v_mov_b32_e32 v113, v111
	v_fmamk_f32 v101, v116, 0xba800000, v101
	v_fmac_f32_e32 v102, 0xba800000, v116
	v_mul_f32_e32 v108, v100, v100
	v_pk_add_f32 v[110:111], v[114:115], v[112:113]
	v_fmamk_f32 v103, v116, 0xba800000, v103
	v_pk_fma_f32 v[112:113], v[100:101], v[100:101], v[108:109] op_sel_hi:[1,1,0]
	v_mul_f32_e32 v108, v102, v102
	v_pk_add_f32 v[110:111], v[110:111], v[110:111] op_sel_hi:[0,1]
	v_pk_fma_f32 v[114:115], v[102:103], v[102:103], v[108:109] op_sel_hi:[1,1,0]
	v_fmamk_f32 v5, v116, 0xba800000, v5
	v_fmamk_f32 v4, v116, 0xba800000, v4
	v_fmamk_f32 v3, v116, 0xba800000, v3
	v_fmac_f32_e32 v2, 0xba800000, v116
	v_mul_f32_e32 v112, v2, v2
	v_mul_f32_e32 v114, v3, v3
	v_mul_f32_e32 v108, v4, v4
	v_mul_f32_e32 v110, v5, v5
	v_pk_add_f32 v[112:113], v[112:113], v[114:115]
	v_pk_add_f32 v[108:109], v[108:109], v[110:111]
	s_nop 0
	v_pk_add_f32 v[108:109], v[112:113], v[108:109]
	s_nop 0
	v_add_f32_e32 v108, v108, v109
	ds_bpermute_b32 v109, v82, v108
	s_waitcnt lgkmcnt(0)
; #define LAS __attribute__((address_space(3)))
; __device__ __forceinline__ unsigned cvt_pk_bf16(float lo, float hi) { unsigned r; asm("v_cvt_pk_bf16_f32 %0, %1, %2" : "=v"(r) : "v"(lo), "v"(hi)); return r; }
; __device__ __forceinline__ float sum4(const f32x4 v) { return (v[0] + v[1]) + (v[2] + v[3]); }
; __device__ __forceinline__ float sq4(const f32x4 v) { return (v[0] * v[0] + v[1] * v[1]) + (v[2] * v[2] + v[3] * v[3]); }
; __device__ __forceinline__ float siluf_(float x) { return x * sigmoidf_(x); }
; __device__ __forceinline__ void phase_convpool(const Ctx& P, LAS unsigned char* lds, int vcu, int G) {
;     ...
;         for (int q = 0; q < 4; ++q) { const int tt = wave * 4 + q; f32x4 v[4]; float s = 0.f;
; #pragma unroll
;             for (int j = 0; j < 4; ++j) { v[j] = *(const LAS f32x4*)(tile + tt * 1024 + 4 * lane + 256 * j); s += sum4(v[j]); }
;             const float mean = wave_sum(s) * (1.0f / 1024.0f); float s2 = 0.f;
; #pragma unroll
;             for (int j = 0; j < 4; ++j) { v[j] = v[j] - mean; s2 += sq4(v[j]); }
;             const float rstd = __builtin_amdgcn_rsqf(wave_sum(s2) * (1.0f / 1024.0f) + EPS);
; #pragma unroll
;             for (int j = 0; j < 4; ++j) { const int c = 4 * lane + 256 * j; const f32x4 g4 = *(const f32x4*)(P.in[13] + c), b4 = *(const f32x4*)(P.in[14] + c); f32x4 y = v[j] * rstd * g4 + b4;
; #pragma unroll
;                 for (int e = 0; e < 4; ++e) y[e] = siluf_(y[e]);
;                 u32x2 w; w.x = cvt_pk_bf16(y[0], y[1]); w.y = cvt_pk_bf16(y[2], y[3]); *(u32x2*)(Y0 + (size_t)(rowbase + t0 + tt) * DM + 1024 + c) = w; } }
	v_add_f32_e32 v108, v108, v109
	ds_bpermute_b32 v109, v83, v108
	s_waitcnt lgkmcnt(0)
	v_add_f32_e32 v108, v108, v109
	ds_bpermute_b32 v109, v84, v108
	s_waitcnt lgkmcnt(0)
	v_add_f32_e32 v108, v108, v109
	ds_bpermute_b32 v109, v85, v108
	s_waitcnt lgkmcnt(0)
	v_add_f32_e32 v108, v108, v109
	ds_bpermute_b32 v109, v86, v108
	s_waitcnt lgkmcnt(0)
	v_add_f32_e32 v108, v108, v109
	ds_bpermute_b32 v109, v87, v108
	s_waitcnt lgkmcnt(0)
	v_add_f32_e32 v108, v108, v109
	v_fmamk_f32 v108, v108, 0x3a800000, v205
	v_rsq_f32_e32 v108, v108
	s_nop 0
	v_pk_mul_f32 v[92:93], v[92:93], v[108:109] op_sel_hi:[1,0]
	v_pk_mul_f32 v[94:95], v[94:95], v[108:109] op_sel_hi:[1,0]
	v_pk_fma_f32 v[88:89], v[104:105], v[92:93], v[88:89]
	v_pk_fma_f32 v[90:91], v[106:107], v[94:95], v[90:91]
	v_mul_f32_e32 v92, 0xbfb8aa3b, v88
	v_mul_f32_e32 v93, 0xbfb8aa3b, v89
	v_exp_f32_e32 v92, v92
	v_exp_f32_e32 v93, v93
	v_mul_f32_e32 v94, 0xbfb8aa3b, v90
	v_mul_f32_e32 v95, 0xbfb8aa3b, v91
	v_exp_f32_e32 v94, v94
	v_exp_f32_e32 v95, v95
	v_add_f32_e32 v92, 1.0, v92
	v_add_f32_e32 v93, 1.0, v93
	v_rcp_f32_e32 v92, v92
	v_rcp_f32_e32 v93, v93
	v_add_f32_e32 v94, 1.0, v94
	v_add_f32_e32 v95, 1.0, v95
	v_rcp_f32_e32 v94, v94
	v_rcp_f32_e32 v95, v95
	v_mul_f32_e32 v88, v88, v92
	v_mul_f32_e32 v89, v89, v93
	v_lshl_add_u64 v[104:105], v[78:79], 0, s[12:13]
	v_mul_f32_e32 v90, v90, v94
	v_mul_f32_e32 v91, v91, v95
	v_cvt_pk_bf16_f32 v88, v88, v89
	v_cvt_pk_bf16_f32 v89, v90, v91
	global_store_dwordx2 v[104:105], v[88:89], off offset:2048
	v_pk_mul_f32 v[96:97], v[96:97], v[108:109] op_sel_hi:[1,0]
	v_pk_mul_f32 v[98:99], v[98:99], v[108:109] op_sel_hi:[1,0]
	v_pk_mul_f32 v[2:3], v[2:3], v[108:109] op_sel_hi:[1,0]
	v_pk_mul_f32 v[4:5], v[4:5], v[108:109] op_sel_hi:[1,0]
	s_waitcnt lgkmcnt(0)
	v_mov_b64_e32 v[92:93], v[226:227]
	v_mov_b64_e32 v[94:95], v[228:229]
	v_mov_b64_e32 v[88:89], v[242:243]
	v_mov_b64_e32 v[90:91], v[244:245]
	v_pk_fma_f32 v[88:89], v[92:93], v[96:97], v[88:89]
	v_pk_fma_f32 v[90:91], v[94:95], v[98:99], v[90:91]
	v_mul_f32_e32 v92, 0xbfb8aa3b, v88
	v_mul_f32_e32 v93, 0xbfb8aa3b, v89
	v_mul_f32_e32 v94, 0xbfb8aa3b, v90
	v_mul_f32_e32 v95, 0xbfb8aa3b, v91
	v_exp_f32_e32 v92, v92
	v_exp_f32_e32 v93, v93
	v_exp_f32_e32 v94, v94
	v_exp_f32_e32 v95, v95
	v_add_f32_e32 v92, 1.0, v92
	v_add_f32_e32 v93, 1.0, v93
	v_add_f32_e32 v94, 1.0, v94
	v_add_f32_e32 v95, 1.0, v95
	v_rcp_f32_e32 v92, v92
	v_rcp_f32_e32 v93, v93
	v_rcp_f32_e32 v94, v94
	v_rcp_f32_e32 v95, v95
	v_mul_f32_e32 v88, v88, v92
	v_mul_f32_e32 v89, v89, v93
	v_mul_f32_e32 v90, v90, v94
	v_mul_f32_e32 v91, v91, v95
	v_cvt_pk_bf16_f32 v88, v88, v89
	v_cvt_pk_bf16_f32 v89, v90, v91
	global_store_dwordx2 v[104:105], v[88:89], off offset:2560
	s_waitcnt lgkmcnt(0)
	v_mov_b64_e32 v[88:89], v[230:231]
	v_mov_b64_e32 v[90:91], v[232:233]
	v_mov_b64_e32 v[92:93], v[246:247]
	v_mov_b64_e32 v[94:95], v[248:249]
	v_pk_mul_f32 v[96:97], v[100:101], v[108:109] op_sel_hi:[1,0]
	v_pk_mul_f32 v[98:99], v[102:103], v[108:109] op_sel_hi:[1,0]
	v_pk_fma_f32 v[88:89], v[88:89], v[96:97], v[92:93]
	v_pk_fma_f32 v[90:91], v[90:91], v[98:99], v[94:95]
	v_mul_f32_e32 v92, 0xbfb8aa3b, v88
	v_mul_f32_e32 v93, 0xbfb8aa3b, v89
	v_mul_f32_e32 v94, 0xbfb8aa3b, v90
	v_mul_f32_e32 v95, 0xbfb8aa3b, v91
	v_exp_f32_e32 v92, v92
	v_exp_f32_e32 v93, v93
	v_exp_f32_e32 v94, v94
	v_exp_f32_e32 v95, v95
	v_add_f32_e32 v92, 1.0, v92
	v_add_f32_e32 v93, 1.0, v93
	v_add_f32_e32 v94, 1.0, v94
	v_add_f32_e32 v95, 1.0, v95
	v_rcp_f32_e32 v92, v92
	v_rcp_f32_e32 v93, v93
	v_rcp_f32_e32 v94, v94
	v_rcp_f32_e32 v95, v95
	v_mul_f32_e32 v88, v88, v92
	v_mul_f32_e32 v89, v89, v93
	v_mul_f32_e32 v90, v90, v94
	v_mul_f32_e32 v91, v91, v95
	v_cvt_pk_bf16_f32 v88, v88, v89
	v_cvt_pk_bf16_f32 v89, v90, v91
	global_store_dwordx2 v[104:105], v[88:89], off offset:3072
	s_waitcnt lgkmcnt(0)
	v_mov_b64_e32 v[88:89], v[234:235]
	v_mov_b64_e32 v[90:91], v[236:237]
	v_mov_b64_e32 v[92:93], v[250:251]
	v_mov_b64_e32 v[94:95], v[252:253]
	v_pk_fma_f32 v[2:3], v[2:3], v[88:89], v[92:93]
	v_pk_fma_f32 v[4:5], v[4:5], v[90:91], v[94:95]
	v_mul_f32_e32 v88, 0xbfb8aa3b, v2
	v_mul_f32_e32 v89, 0xbfb8aa3b, v3
	v_mul_f32_e32 v90, 0xbfb8aa3b, v4
	v_mul_f32_e32 v91, 0xbfb8aa3b, v5
	v_exp_f32_e32 v88, v88
	v_exp_f32_e32 v89, v89
	v_exp_f32_e32 v90, v90
	v_exp_f32_e32 v91, v91
	v_add_f32_e32 v88, 1.0, v88
	v_add_f32_e32 v89, 1.0, v89
	v_add_f32_e32 v90, 1.0, v90
	v_add_f32_e32 v91, 1.0, v91
	v_rcp_f32_e32 v88, v88
	v_rcp_f32_e32 v89, v89
	v_rcp_f32_e32 v90, v90
	v_rcp_f32_e32 v91, v91
	v_mul_f32_e32 v2, v2, v88
	v_mul_f32_e32 v3, v3, v89
	v_mul_f32_e32 v4, v4, v90
	v_mul_f32_e32 v5, v5, v91
	v_cvt_pk_bf16_f32 v2, v2, v3
	v_cvt_pk_bf16_f32 v3, v4, v5
	global_store_dwordx2 v[104:105], v[2:3], off offset:3584
	v_add_u32_e32 v2, s25, v188
	ds_read_b128 v[92:95], v2
	ds_read_b128 v[96:99], v2 offset:1024
	ds_read_b128 v[100:103], v2 offset:2048
	ds_read_b128 v[2:5], v2 offset:3072
	s_waitcnt lgkmcnt(0)
	v_mov_b32_e32 v104, v93
	v_mov_b32_e32 v105, v94
	v_mov_b32_e32 v106, v92
	v_mov_b32_e32 v107, v95
	v_mov_b32_e32 v108, v97
	v_mov_b32_e32 v109, v98
	v_mov_b32_e32 v110, v96
	v_mov_b32_e32 v111, v99
	v_pk_add_f32 v[104:105], v[104:105], v[106:107]
	v_pk_add_f32 v[106:107], v[108:109], v[110:111]
	v_add_f32_e32 v110, v104, v105
	v_pk_add_f32 v[104:105], v[106:107], v[106:107] op_sel:[0,1] op_sel_hi:[1,0]
	v_add_f32_e32 v112, v100, v101
	v_add_f32_e32 v114, v102, v103
	v_mov_b32_e32 v117, v2
	v_mov_b32_e32 v113, v4
	v_mov_b32_e32 v115, v5
	v_add_f32_e32 v116, 0, v110
	v_mov_b32_e32 v105, v3
	v_pk_add_f32 v[108:109], v[112:113], v[114:115]
	v_pk_add_f32 v[104:105], v[116:117], v[104:105]
	v_pk_add_f32 v[104:105], v[104:105], v[108:109]
	s_nop 0
	v_add_f32_e32 v104, v104, v105
	ds_bpermute_b32 v105, v82, v104
	s_waitcnt lgkmcnt(0)
; #define LAS __attribute__((address_space(3)))
; __device__ __forceinline__ unsigned cvt_pk_bf16(float lo, float hi) { unsigned r; asm("v_cvt_pk_bf16_f32 %0, %1, %2" : "=v"(r) : "v"(lo), "v"(hi)); return r; }
; __device__ __forceinline__ float sum4(const f32x4 v) { return (v[0] + v[1]) + (v[2] + v[3]); }
; __device__ __forceinline__ float sq4(const f32x4 v) { return (v[0] * v[0] + v[1] * v[1]) + (v[2] * v[2] + v[3] * v[3]); }
; __device__ __forceinline__ float siluf_(float x) { return x * sigmoidf_(x); }
; __device__ __forceinline__ void phase_convpool(const Ctx& P, LAS unsigned char* lds, int vcu, int G) {
;     ...
;         for (int q = 0; q < 4; ++q) { const int tt = wave * 4 + q; f32x4 v[4]; float s = 0.f;
; #pragma unroll
;             for (int j = 0; j < 4; ++j) { v[j] = *(const LAS f32x4*)(tile + tt * 1024 + 4 * lane + 256 * j); s += sum4(v[j]); }
;             const float mean = wave_sum(s) * (1.0f / 1024.0f); float s2 = 0.f;
; #pragma unroll
;             for (int j = 0; j < 4; ++j) { v[j] = v[j] - mean; s2 += sq4(v[j]); }
;             const float rstd = __builtin_amdgcn_rsqf(wave_sum(s2) * (1.0f / 1024.0f) + EPS);
; #pragma unroll
;             for (int j = 0; j < 4; ++j) { const int c = 4 * lane + 256 * j; const f32x4 g4 = *(const f32x4*)(P.in[13] + c), b4 = *(const f32x4*)(P.in[14] + c); f32x4 y = v[j] * rstd * g4 + b4;
; #pragma unroll
;                 for (int e = 0; e < 4; ++e) y[e] = siluf_(y[e]);
;                 u32x2 w; w.x = cvt_pk_bf16(y[0], y[1]); w.y = cvt_pk_bf16(y[2], y[3]); *(u32x2*)(Y0 + (size_t)(rowbase + t0 + tt) * DM + 1024 + c) = w; } }
	v_add_f32_e32 v104, v104, v105
	ds_bpermute_b32 v105, v83, v104
	s_waitcnt lgkmcnt(0)
	v_add_f32_e32 v104, v104, v105
	ds_bpermute_b32 v105, v84, v104
	s_waitcnt lgkmcnt(0)
	v_add_f32_e32 v104, v104, v105
	ds_bpermute_b32 v105, v85, v104
	s_waitcnt lgkmcnt(0)
	v_add_f32_e32 v104, v104, v105
	ds_bpermute_b32 v105, v86, v104
	s_waitcnt lgkmcnt(0)
	v_add_f32_e32 v104, v104, v105
	ds_bpermute_b32 v105, v87, v104
	s_waitcnt lgkmcnt(0)
	v_add_f32_e32 v108, v104, v105
	v_mov_b64_e32 v[88:89], v[222:223]
	v_mov_b64_e32 v[90:91], v[224:225]
	s_nop 0
	v_mov_b64_e32 v[104:105], v[238:239]
	v_mov_b64_e32 v[106:107], v[240:241]
	v_fmamk_f32 v93, v108, 0xba800000, v93
	v_fmamk_f32 v92, v108, 0xba800000, v92
	v_fmamk_f32 v95, v108, 0xba800000, v95
	v_fmac_f32_e32 v94, 0xba800000, v108
	v_fmamk_f32 v97, v108, 0xba800000, v97
	v_fmamk_f32 v96, v108, 0xba800000, v96
	v_fmamk_f32 v99, v108, 0xba800000, v99
	v_fmac_f32_e32 v98, 0xba800000, v108
	v_fmamk_f32 v101, v108, 0xba800000, v101
	v_fmamk_f32 v100, v108, 0xba800000, v100
	v_fmamk_f32 v103, v108, 0xba800000, v103
	v_fmac_f32_e32 v102, 0xba800000, v108
	v_fmamk_f32 v5, v108, 0xba800000, v5
	v_fmamk_f32 v4, v108, 0xba800000, v4
	v_fmamk_f32 v3, v108, 0xba800000, v3
	v_fmac_f32_e32 v2, 0xba800000, v108
	v_pk_mul_f32 v[108:109], v[94:95], v[94:95]
	v_pk_mul_f32 v[110:111], v[92:93], v[92:93]
	v_pk_mul_f32 v[112:113], v[98:99], v[98:99]
	v_pk_mul_f32 v[114:115], v[96:97], v[96:97]
	v_pk_mov_b32 v[120:121], v[110:111], v[108:109] op_sel:[1,0]
	v_mov_b32_e32 v111, v109
	v_pk_mov_b32 v[108:109], v[114:115], v[112:113] op_sel:[1,0]
	v_mov_b32_e32 v115, v113
	v_mul_f32_e32 v116, v100, v100
	v_mul_f32_e32 v118, v102, v102
	v_pk_add_f32 v[110:111], v[120:121], v[110:111]
	v_pk_add_f32 v[108:109], v[108:109], v[114:115]
	v_pk_fma_f32 v[112:113], v[100:101], v[100:101], v[116:117] op_sel_hi:[1,1,0]
	v_pk_fma_f32 v[116:117], v[102:103], v[102:103], v[118:119] op_sel_hi:[1,1,0]
	v_pk_add_f32 v[110:111], v[110:111], v[110:111] op_sel_hi:[0,1]
	v_pk_add_f32 v[108:109], v[108:109], v[108:109] op_sel_hi:[0,1]
	v_mul_f32_e32 v112, v2, v2
	v_mul_f32_e32 v116, v3, v3
	v_mul_f32_e32 v110, v4, v4
	v_mul_f32_e32 v108, v5, v5
	v_pk_add_f32 v[112:113], v[112:113], v[116:117]
	v_pk_add_f32 v[108:109], v[110:111], v[108:109]
	v_lshl_add_u64 v[110:111], v[78:79], 0, s[10:11]
	v_pk_add_f32 v[108:109], v[112:113], v[108:109]
	s_nop 0
	v_add_f32_e32 v108, v108, v109
	ds_bpermute_b32 v82, v82, v108
	s_waitcnt lgkmcnt(0)
	v_add_f32_e32 v82, v108, v82
	ds_bpermute_b32 v83, v83, v82
	s_waitcnt lgkmcnt(0)
	v_add_f32_e32 v82, v82, v83
	ds_bpermute_b32 v83, v84, v82
	s_waitcnt lgkmcnt(0)
	v_add_f32_e32 v82, v82, v83
	ds_bpermute_b32 v83, v85, v82
	s_waitcnt lgkmcnt(0)
	v_add_f32_e32 v82, v82, v83
	ds_bpermute_b32 v83, v86, v82
	s_waitcnt lgkmcnt(0)
	v_add_f32_e32 v82, v82, v83
	ds_bpermute_b32 v83, v87, v82
	s_waitcnt lgkmcnt(0)
	v_add_f32_e32 v82, v82, v83
	v_fmamk_f32 v82, v82, 0x3a800000, v205
	v_rsq_f32_e32 v108, v82
	s_nop 0
	v_pk_mul_f32 v[82:83], v[92:93], v[108:109] op_sel_hi:[1,0]
	v_pk_mul_f32 v[84:85], v[94:95], v[108:109] op_sel_hi:[1,0]
	v_pk_fma_f32 v[82:83], v[88:89], v[82:83], v[104:105]
	v_pk_fma_f32 v[84:85], v[90:91], v[84:85], v[106:107]
	v_mul_f32_e32 v86, 0xbfb8aa3b, v82
	v_mul_f32_e32 v87, 0xbfb8aa3b, v83
	v_mul_f32_e32 v88, 0xbfb8aa3b, v84
	v_mul_f32_e32 v89, 0xbfb8aa3b, v85
	v_exp_f32_e32 v86, v86
	v_exp_f32_e32 v87, v87
	v_exp_f32_e32 v88, v88
	v_exp_f32_e32 v89, v89
	v_add_f32_e32 v86, 1.0, v86
	v_add_f32_e32 v87, 1.0, v87
	v_add_f32_e32 v88, 1.0, v88
	v_add_f32_e32 v89, 1.0, v89
	v_rcp_f32_e32 v86, v86
	v_rcp_f32_e32 v87, v87
	v_rcp_f32_e32 v88, v88
	v_rcp_f32_e32 v89, v89
	v_mul_f32_e32 v82, v82, v86
	v_mul_f32_e32 v83, v83, v87
	v_mul_f32_e32 v84, v84, v88
	v_mul_f32_e32 v85, v85, v89
	v_cvt_pk_bf16_f32 v82, v82, v83
	v_cvt_pk_bf16_f32 v83, v84, v85
	global_store_dwordx2 v[110:111], v[82:83], off offset:2048
	v_pk_mul_f32 v[2:3], v[2:3], v[108:109] op_sel_hi:[1,0]
	v_pk_mul_f32 v[4:5], v[4:5], v[108:109] op_sel_hi:[1,0]
	s_waitcnt lgkmcnt(0)
; __device__ __forceinline__ unsigned cvt_pk_bf16(float lo, float hi) { unsigned r; asm("v_cvt_pk_bf16_f32 %0, %1, %2" : "=v"(r) : "v"(lo), "v"(hi)); return r; }
; __device__ __forceinline__ float siluf_(float x) { return x * sigmoidf_(x); }
; __device__ __forceinline__ void phase_convpool(const Ctx& P, LAS unsigned char* lds, int vcu, int G) {
;     ...
; #pragma unroll
;             for (int j = 0; j < 4; ++j) { const int c = 4 * lane + 256 * j; const f32x4 g4 = *(const f32x4*)(P.in[13] + c), b4 = *(const f32x4*)(P.in[14] + c); f32x4 y = v[j] * rstd * g4 + b4;
; #pragma unroll
;                 for (int e = 0; e < 4; ++e) y[e] = siluf_(y[e]);
;                 u32x2 w; w.x = cvt_pk_bf16(y[0], y[1]); w.y = cvt_pk_bf16(y[2], y[3]); *(u32x2*)(Y0 + (size_t)(rowbase + t0 + tt) * DM + 1024 + c) = w; } }
;         __syncthreads();
	v_mov_b64_e32 v[82:83], v[226:227]
	v_mov_b64_e32 v[84:85], v[228:229]
	v_mov_b64_e32 v[86:87], v[242:243]
	v_mov_b64_e32 v[88:89], v[244:245]
	v_pk_mul_f32 v[90:91], v[96:97], v[108:109] op_sel_hi:[1,0]
	v_pk_mul_f32 v[92:93], v[98:99], v[108:109] op_sel_hi:[1,0]
	v_pk_fma_f32 v[82:83], v[82:83], v[90:91], v[86:87]
	v_pk_fma_f32 v[84:85], v[84:85], v[92:93], v[88:89]
	v_mul_f32_e32 v86, 0xbfb8aa3b, v82
	v_mul_f32_e32 v87, 0xbfb8aa3b, v83
	v_mul_f32_e32 v88, 0xbfb8aa3b, v84
	v_mul_f32_e32 v89, 0xbfb8aa3b, v85
	v_exp_f32_e32 v86, v86
	v_exp_f32_e32 v87, v87
	v_exp_f32_e32 v88, v88
	v_exp_f32_e32 v89, v89
	v_add_f32_e32 v86, 1.0, v86
	v_add_f32_e32 v87, 1.0, v87
	v_add_f32_e32 v88, 1.0, v88
	v_add_f32_e32 v89, 1.0, v89
	v_rcp_f32_e32 v86, v86
	v_rcp_f32_e32 v87, v87
	v_rcp_f32_e32 v88, v88
	v_rcp_f32_e32 v89, v89
	v_mul_f32_e32 v82, v82, v86
	v_mul_f32_e32 v83, v83, v87
	v_mul_f32_e32 v84, v84, v88
	v_mul_f32_e32 v85, v85, v89
	v_cvt_pk_bf16_f32 v82, v82, v83
	v_cvt_pk_bf16_f32 v83, v84, v85
	global_store_dwordx2 v[110:111], v[82:83], off offset:2560
	s_waitcnt lgkmcnt(0)
	v_mov_b64_e32 v[82:83], v[230:231]
	v_mov_b64_e32 v[84:85], v[232:233]
	v_mov_b64_e32 v[86:87], v[246:247]
	v_mov_b64_e32 v[88:89], v[248:249]
	v_pk_mul_f32 v[90:91], v[100:101], v[108:109] op_sel_hi:[1,0]
	v_pk_mul_f32 v[92:93], v[102:103], v[108:109] op_sel_hi:[1,0]
	v_pk_fma_f32 v[82:83], v[82:83], v[90:91], v[86:87]
	v_pk_fma_f32 v[84:85], v[84:85], v[92:93], v[88:89]
	v_mul_f32_e32 v86, 0xbfb8aa3b, v82
	v_mul_f32_e32 v87, 0xbfb8aa3b, v83
	v_mul_f32_e32 v88, 0xbfb8aa3b, v84
	v_mul_f32_e32 v89, 0xbfb8aa3b, v85
	v_exp_f32_e32 v86, v86
	v_exp_f32_e32 v87, v87
	v_exp_f32_e32 v88, v88
	v_exp_f32_e32 v89, v89
	v_add_f32_e32 v86, 1.0, v86
	v_add_f32_e32 v87, 1.0, v87
	v_add_f32_e32 v88, 1.0, v88
	v_add_f32_e32 v89, 1.0, v89
	v_rcp_f32_e32 v86, v86
	v_rcp_f32_e32 v87, v87
	v_rcp_f32_e32 v88, v88
	v_rcp_f32_e32 v89, v89
	v_mul_f32_e32 v82, v82, v86
	v_mul_f32_e32 v83, v83, v87
	v_mul_f32_e32 v84, v84, v88
	v_mul_f32_e32 v85, v85, v89
	v_cvt_pk_bf16_f32 v82, v82, v83
	v_cvt_pk_bf16_f32 v83, v84, v85
	global_store_dwordx2 v[110:111], v[82:83], off offset:3072
	s_waitcnt lgkmcnt(0)
	v_mov_b64_e32 v[80:81], v[234:235]
	v_mov_b64_e32 v[82:83], v[236:237]
	v_mov_b64_e32 v[84:85], v[250:251]
	v_mov_b64_e32 v[86:87], v[252:253]
	v_pk_fma_f32 v[2:3], v[2:3], v[80:81], v[84:85]
	v_pk_fma_f32 v[4:5], v[4:5], v[82:83], v[86:87]
	v_mul_f32_e32 v80, 0xbfb8aa3b, v2
	v_mul_f32_e32 v81, 0xbfb8aa3b, v3
	v_mul_f32_e32 v82, 0xbfb8aa3b, v4
	v_mul_f32_e32 v83, 0xbfb8aa3b, v5
	v_exp_f32_e32 v80, v80
	v_exp_f32_e32 v81, v81
	v_exp_f32_e32 v82, v82
	v_exp_f32_e32 v83, v83
	v_add_f32_e32 v80, 1.0, v80
	v_add_f32_e32 v81, 1.0, v81
	v_add_f32_e32 v82, 1.0, v82
	v_add_f32_e32 v83, 1.0, v83
	v_rcp_f32_e32 v80, v80
	v_rcp_f32_e32 v81, v81
	v_rcp_f32_e32 v82, v82
	v_rcp_f32_e32 v83, v83
	v_mul_f32_e32 v2, v2, v80
	v_mul_f32_e32 v3, v3, v81
	v_mul_f32_e32 v4, v4, v82
	v_mul_f32_e32 v5, v5, v83
	v_cvt_pk_bf16_f32 v2, v2, v3
	v_cvt_pk_bf16_f32 v3, v4, v5
	global_store_dwordx2 v[110:111], v[2:3], off offset:3584
	s_barrier
	s_cbranch_scc0 .LBB0_1122
